# speedup vs baseline: 1.0131x; 1.0131x over previous
_Z12quant_kernelPKfS0_PKiPhS3_PjS4_PfS5_S5_Pi:
	s_cmp_eq_u32 s2, 0
	s_cbranch_scc0 .Lq_nopub
	s_load_dwordx2 s[40:41], s[0:1], 0x50
	s_load_dwordx4 s[44:47], s[0:1], 0x0
	s_load_dwordx2 s[48:49], s[0:1], 0x10
	s_waitcnt lgkmcnt(0)
	s_add_u32 s40, s40, 0x4040
	s_addc_u32 s41, s41, 0
	v_mov_b32_e32 v2, s44
	v_mov_b32_e32 v3, s45
	v_mov_b32_e32 v4, s46
	v_mov_b32_e32 v5, s47
	v_mov_b32_e32 v6, 0
	v_mov_b32_e32 v8, s48
	v_mov_b32_e32 v9, s49
	global_store_dwordx4 v6, v[2:5], s[40:41]
	global_store_dwordx2 v6, v[8:9], s[40:41] offset:16
	s_nop 3
.Lq_nopub:
	s_load_dwordx4 s[12:15], s[0:1], 0x0
	v_or_b32_e32 v1, s2, v0
	v_cmp_eq_u32_e32 vcc, 0, v1
	s_and_saveexec_b64 s[4:5], vcc
	s_cbranch_execz .LBB0_2
	s_load_dwordx2 s[6:7], s[0:1], 0x40
	v_mov_b32_e32 v1, 0
	s_waitcnt lgkmcnt(0)
	global_store_dword v1, v1, s[6:7]

.LBB0_4:
	s_cmpk_gt_i32 s2, 0x7f
	s_cselect_b64 s[16:17], -1, 0
	s_add_i32 s3, s2, 0xffffff80
	s_cmpk_lt_i32 s2, 0x80
	s_cselect_b64 s[8:9], -1, 0
	s_and_b64 s[10:11], s[8:9], exec
	s_cselect_b32 s10, s2, s3
	s_waitcnt lgkmcnt(0)
	s_cselect_b32 s23, s13, s15
	s_cselect_b32 s22, s12, s14
	s_ashr_i32 s11, s10, 31
	v_lshrrev_b32_e32 v157, 3, v0
	s_lshl_b64 s[20:21], s[10:11], 5
	v_and_b32_e32 v162, 24, v157
	v_or_b32_e32 v146, s20, v162
	v_mov_b32_e32 v147, s21
	v_and_b32_e32 v2, 63, v0
	v_lshlrev_b64 v[4:5], 13, v[146:147]
	v_lshl_add_u64 v[4:5], s[22:23], 0, v[4:5]
	v_mov_b32_e32 v143, 0
	v_lshlrev_b32_e32 v142, 4, v2
	v_lshl_add_u64 v[4:5], v[4:5], 0, v[142:143]
	s_movk_i32 s10, 0x1000
	v_add_co_u32_e32 v6, vcc, s10, v4
	s_movk_i32 s10, 0x2000
	s_nop 0
	v_addc_co_u32_e32 v7, vcc, 0, v5, vcc
	v_add_co_u32_e32 v8, vcc, s10, v4
	s_mov_b64 s[10:11], 0x2000
	s_nop 0
	v_addc_co_u32_e32 v9, vcc, 0, v5, vcc
	global_load_dwordx4 v[126:129], v[4:5], off nt
	global_load_dwordx4 v[122:125], v[4:5], off offset:1024 nt
	global_load_dwordx4 v[114:117], v[4:5], off offset:2048 nt
	global_load_dwordx4 v[110:113], v[4:5], off offset:3072 nt
	global_load_dwordx4 v[106:109], v[6:7], off offset:1024 nt
	global_load_dwordx4 v[102:105], v[6:7], off offset:2048 nt
	v_lshl_add_u64 v[10:11], v[4:5], 0, s[10:11]
	global_load_dwordx4 v[118:121], v[8:9], off offset:-4096 nt
	global_load_dwordx4 v[94:97], v[8:9], off nt
	global_load_dwordx4 v[98:101], v[6:7], off offset:3072 nt
	global_load_dwordx4 v[90:93], v[10:11], off offset:1024 nt
	global_load_dwordx4 v[86:89], v[10:11], off offset:2048 nt
	global_load_dwordx4 v[78:81], v[10:11], off offset:3072 nt
	v_add_co_u32_e32 v4, vcc, 0x3000, v4
	v_lshl_add_u64 v[144:145], s[14:15], 0, v[142:143]
	s_nop 0
	v_addc_co_u32_e32 v5, vcc, 0, v5, vcc
	global_load_dwordx4 v[82:85], v[4:5], off nt
	global_load_dwordx4 v[74:77], v[4:5], off offset:1024 nt
	global_load_dwordx4 v[70:73], v[4:5], off offset:2048 nt
	global_load_dwordx4 v[66:69], v[4:5], off offset:3072 nt
	s_and_b64 vcc, exec, s[16:17]
	v_lshl_add_u64 v[148:149], v[146:147], 2, s[18:19]
	v_mov_b32_e32 v35, v143
	v_mov_b32_e32 v36, v143
	v_mov_b32_e32 v37, v143
	v_mov_b32_e32 v38, v143
	v_mov_b32_e32 v39, v143
	v_mov_b32_e32 v40, v143
	v_mov_b32_e32 v41, v143
	v_mov_b32_e32 v42, v143
	v_mov_b32_e32 v43, v143
	v_mov_b32_e32 v44, v143
	v_mov_b32_e32 v45, v143
	v_mov_b32_e32 v46, v143
	v_mov_b32_e32 v47, v143
	v_mov_b32_e32 v48, v143
	v_mov_b32_e32 v49, v143
	v_mov_b32_e32 v50, v143
	v_mov_b32_e32 v51, v143
	v_mov_b32_e32 v52, v143
	v_mov_b32_e32 v53, v143
	v_mov_b32_e32 v54, v143
	v_mov_b32_e32 v55, v143
	v_mov_b32_e32 v56, v143
	v_mov_b32_e32 v57, v143
	v_mov_b32_e32 v58, v143
	v_mov_b32_e32 v59, v143
	v_mov_b32_e32 v60, v143
	v_mov_b32_e32 v61, v143
	v_mov_b32_e32 v62, v143
	v_mov_b32_e32 v63, v143
	v_mov_b32_e32 v64, v143
	v_mov_b32_e32 v65, v143
	s_branch .LBB0_6
	global_load_dword v1, v[148:149], off
	v_mov_b32_e32 v3, 0x7cff
	v_mov_b32_e32 v5, 0
	s_waitcnt vmcnt(0)
	v_med3_i32 v1, v1, 0, v3
	v_lshlrev_b32_e32 v4, 13, v1
	v_lshl_add_u64 v[4:5], v[144:145], 0, v[4:5]
	global_load_dwordx4 v[34:37], v[4:5], off nt
	global_load_dwordx4 v[38:41], v[4:5], off offset:1024 nt
	global_load_dwordx4 v[42:45], v[4:5], off offset:2048 nt
	global_load_dwordx4 v[46:49], v[4:5], off offset:3072 nt
	v_add_co_u32_e32 v4, vcc, 0x1000, v4
	s_waitcnt vmcnt(3)
	v_mov_b32_e32 v143, v34
	v_addc_co_u32_e32 v5, vcc, 0, v5, vcc
	global_load_dwordx4 v[50:53], v[4:5], off nt
	global_load_dwordx4 v[54:57], v[4:5], off offset:1024 nt
	global_load_dwordx4 v[58:61], v[4:5], off offset:2048 nt
	global_load_dwordx4 v[62:65], v[4:5], off offset:3072 nt

.LBB0_13:
	s_branch .LBB0_16
	v_fma_f32 v2, v126, v143, 0
	v_fmac_f32_e32 v2, v127, v35
	v_fmac_f32_e32 v2, v128, v36
	v_fmac_f32_e32 v2, v129, v37
	s_waitcnt vmcnt(6)
	v_fmac_f32_e32 v2, v122, v38
	v_fmac_f32_e32 v2, v123, v39
	v_fmac_f32_e32 v2, v124, v40
	v_fmac_f32_e32 v2, v125, v41
	s_waitcnt vmcnt(5)
	v_fmac_f32_e32 v2, v114, v42
	v_fmac_f32_e32 v2, v115, v43
	v_fmac_f32_e32 v2, v116, v44
	v_fmac_f32_e32 v2, v117, v45
	s_waitcnt vmcnt(4)
	v_fmac_f32_e32 v2, v110, v46
	v_fmac_f32_e32 v2, v111, v47
	v_fmac_f32_e32 v2, v112, v48
	v_fmac_f32_e32 v2, v113, v49
	s_waitcnt vmcnt(3)
	v_fmac_f32_e32 v2, v118, v50
	v_fmac_f32_e32 v2, v119, v51
	v_fmac_f32_e32 v2, v120, v52
	v_fmac_f32_e32 v2, v121, v53
	s_waitcnt vmcnt(2)
	v_fmac_f32_e32 v2, v106, v54
	v_fmac_f32_e32 v2, v107, v55
	v_fmac_f32_e32 v2, v108, v56
	v_fmac_f32_e32 v2, v109, v57
	s_waitcnt vmcnt(1)
	v_fmac_f32_e32 v2, v102, v58
	v_fmac_f32_e32 v2, v103, v59
	v_fmac_f32_e32 v2, v104, v60
	v_fmac_f32_e32 v2, v105, v61
	s_waitcnt vmcnt(0)
	v_fmac_f32_e32 v2, v98, v62
	v_fmac_f32_e32 v2, v99, v63
	v_fmac_f32_e32 v2, v100, v64
	v_fmac_f32_e32 v2, v101, v65
	ds_bpermute_b32 v3, v1, v2
	s_waitcnt lgkmcnt(0)
	v_add_f32_e32 v2, v2, v3
	ds_bpermute_b32 v3, v152, v2
	s_waitcnt lgkmcnt(0)
	v_add_f32_e32 v2, v2, v3
	ds_bpermute_b32 v3, v153, v2
	s_waitcnt lgkmcnt(0)
	v_add_f32_e32 v2, v2, v3
	ds_bpermute_b32 v3, v154, v2
	s_waitcnt lgkmcnt(0)
	v_add_f32_e32 v2, v2, v3
	ds_bpermute_b32 v3, v155, v2
	s_waitcnt lgkmcnt(0)
	v_add_f32_e32 v2, v2, v3
	ds_bpermute_b32 v3, v156, v2
	s_and_saveexec_b64 s[8:9], s[10:11]
	s_cbranch_execz .LBB0_15
	v_lshl_add_u64 v[4:5], v[146:147], 2, s[12:13]
	s_waitcnt lgkmcnt(0)
	v_add_f32_e32 v2, v2, v3
	global_store_dword v[4:5], v2, off

.LBB0_16:
	v_or_b32_e32 v122, 1, v162
	v_mov_b32_e32 v123, 0
	s_waitcnt lgkmcnt(0)
	v_lshl_add_u64 v[2:3], s[20:21], 0, v[122:123]
	v_lshlrev_b64 v[2:3], 13, v[2:3]
	v_lshl_add_u64 v[2:3], s[22:23], 0, v[2:3]
	v_mov_b32_e32 v4, v142
	v_mov_b32_e32 v5, v123
	v_lshl_add_u64 v[2:3], v[2:3], 0, v[4:5]
	v_add_co_u32_e32 v6, vcc, 0x2000, v2
	s_mov_b64 s[8:9], 0x2000
	s_nop 0
	v_addc_co_u32_e32 v7, vcc, 0, v3, vcc
	v_lshl_add_u64 v[4:5], v[2:3], 0, s[8:9]
	v_add_co_u32_e32 v2, vcc, 0x3000, v2
	global_load_dwordx4 v[126:129], v[4:5], off offset:1024 nt
	global_load_dwordx4 v[118:121], v[4:5], off offset:2048 nt
	global_load_dwordx4 v[134:137], v[6:7], off nt
	global_load_dwordx4 v[110:113], v[4:5], off offset:3072 nt
	v_addc_co_u32_e32 v3, vcc, 0, v3, vcc
	global_load_dwordx4 v[114:117], v[2:3], off nt
	global_load_dwordx4 v[106:109], v[2:3], off offset:1024 nt
	global_load_dwordx4 v[102:105], v[2:3], off offset:2048 nt
	global_load_dwordx4 v[98:101], v[2:3], off offset:3072 nt
	s_and_b64 vcc, exec, s[6:7]
	s_branch .LBB0_18
	global_load_dword v2, v[148:149], off offset:4
	v_mov_b32_e32 v4, 0x7cff
	v_mov_b32_e32 v3, v123
	s_waitcnt vmcnt(0)
	v_med3_i32 v2, v2, 0, v4
	v_lshlrev_b32_e32 v2, 13, v2
	v_lshl_add_u64 v[2:3], v[144:145], 0, v[2:3]
	global_load_dwordx4 v[34:37], v[2:3], off nt
	global_load_dwordx4 v[38:41], v[2:3], off offset:1024 nt
	global_load_dwordx4 v[42:45], v[2:3], off offset:2048 nt
	global_load_dwordx4 v[46:49], v[2:3], off offset:3072 nt
	v_add_co_u32_e32 v2, vcc, 0x1000, v2
	s_waitcnt vmcnt(3)
	v_mov_b32_e32 v143, v34
	v_addc_co_u32_e32 v3, vcc, 0, v3, vcc
	global_load_dwordx4 v[50:53], v[2:3], off nt
	global_load_dwordx4 v[54:57], v[2:3], off offset:1024 nt
	global_load_dwordx4 v[58:61], v[2:3], off offset:2048 nt
	global_load_dwordx4 v[62:65], v[2:3], off offset:3072 nt

.LBB0_25:
	s_branch .LBB0_28
	v_fma_f32 v2, v94, v143, 0
	v_fmac_f32_e32 v2, v95, v35
	v_fmac_f32_e32 v2, v96, v36
	v_fmac_f32_e32 v2, v97, v37
	s_waitcnt vmcnt(6)
	v_fmac_f32_e32 v2, v90, v38
	v_fmac_f32_e32 v2, v91, v39
	v_fmac_f32_e32 v2, v92, v40
	v_fmac_f32_e32 v2, v93, v41
	s_waitcnt vmcnt(5)
	v_fmac_f32_e32 v2, v86, v42
	v_fmac_f32_e32 v2, v87, v43
	v_fmac_f32_e32 v2, v88, v44
	v_fmac_f32_e32 v2, v89, v45
	s_waitcnt vmcnt(4)
	v_fmac_f32_e32 v2, v78, v46
	v_fmac_f32_e32 v2, v79, v47
	v_fmac_f32_e32 v2, v80, v48
	v_fmac_f32_e32 v2, v81, v49
	s_waitcnt vmcnt(3)
	v_fmac_f32_e32 v2, v82, v50
	v_fmac_f32_e32 v2, v83, v51
	v_fmac_f32_e32 v2, v84, v52
	v_fmac_f32_e32 v2, v85, v53
	s_waitcnt vmcnt(2)
	v_fmac_f32_e32 v2, v74, v54
	v_fmac_f32_e32 v2, v75, v55
	v_fmac_f32_e32 v2, v76, v56
	v_fmac_f32_e32 v2, v77, v57
	s_waitcnt vmcnt(1)
	v_fmac_f32_e32 v2, v70, v58
	v_fmac_f32_e32 v2, v71, v59
	v_fmac_f32_e32 v2, v72, v60
	v_fmac_f32_e32 v2, v73, v61
	s_waitcnt vmcnt(0)
	v_fmac_f32_e32 v2, v66, v62
	v_fmac_f32_e32 v2, v67, v63
	v_fmac_f32_e32 v2, v68, v64
	v_fmac_f32_e32 v2, v69, v65
	ds_bpermute_b32 v3, v1, v2
	s_waitcnt lgkmcnt(0)
	v_add_f32_e32 v2, v2, v3
	ds_bpermute_b32 v3, v152, v2
	s_waitcnt lgkmcnt(0)
	v_add_f32_e32 v2, v2, v3
	ds_bpermute_b32 v3, v153, v2
	s_waitcnt lgkmcnt(0)
	v_add_f32_e32 v2, v2, v3
	ds_bpermute_b32 v3, v154, v2
	s_waitcnt lgkmcnt(0)
	v_add_f32_e32 v2, v2, v3
	ds_bpermute_b32 v3, v155, v2
	s_waitcnt lgkmcnt(0)
	v_add_f32_e32 v2, v2, v3
	ds_bpermute_b32 v3, v156, v2
	s_and_saveexec_b64 s[8:9], s[10:11]
	s_cbranch_execz .LBB0_27
	v_lshl_add_u64 v[4:5], v[146:147], 2, s[12:13]
	s_waitcnt lgkmcnt(0)
	v_add_f32_e32 v2, v2, v3
	global_store_dword v[4:5], v2, off offset:4

.LBB0_28:
	v_or_b32_e32 v70, 2, v162
	v_mov_b32_e32 v71, 0
	s_waitcnt lgkmcnt(0)
	v_lshl_add_u64 v[2:3], s[20:21], 0, v[70:71]
	v_lshlrev_b64 v[2:3], 13, v[2:3]
	v_lshl_add_u64 v[2:3], s[22:23], 0, v[2:3]
	v_mov_b32_e32 v4, v142
	v_mov_b32_e32 v5, v71
	v_lshl_add_u64 v[2:3], v[2:3], 0, v[4:5]
	v_add_co_u32_e32 v6, vcc, 0x2000, v2
	s_mov_b64 s[8:9], 0x2000
	s_nop 0
	v_addc_co_u32_e32 v7, vcc, 0, v3, vcc
	v_lshl_add_u64 v[4:5], v[2:3], 0, s[8:9]
	v_add_co_u32_e32 v2, vcc, 0x3000, v2
	global_load_dwordx4 v[130:133], v[4:5], off offset:1024 nt
	global_load_dwordx4 v[122:125], v[4:5], off offset:2048 nt
	global_load_dwordx4 v[138:141], v[6:7], off nt
	global_load_dwordx4 v[90:93], v[4:5], off offset:3072 nt
	v_addc_co_u32_e32 v3, vcc, 0, v3, vcc
	global_load_dwordx4 v[94:97], v[2:3], off nt
	global_load_dwordx4 v[82:85], v[2:3], off offset:1024 nt
	global_load_dwordx4 v[74:77], v[2:3], off offset:2048 nt
	global_load_dwordx4 v[66:69], v[2:3], off offset:3072 nt
	s_and_b64 vcc, exec, s[6:7]
	s_branch .LBB0_30
	global_load_dword v2, v[148:149], off offset:8
	v_mov_b32_e32 v4, 0x7cff
	v_mov_b32_e32 v3, v71
	s_waitcnt vmcnt(0)
	v_med3_i32 v2, v2, 0, v4
	v_lshlrev_b32_e32 v2, 13, v2
	v_lshl_add_u64 v[2:3], v[144:145], 0, v[2:3]
	global_load_dwordx4 v[34:37], v[2:3], off nt
	global_load_dwordx4 v[38:41], v[2:3], off offset:1024 nt
	global_load_dwordx4 v[42:45], v[2:3], off offset:2048 nt
	global_load_dwordx4 v[46:49], v[2:3], off offset:3072 nt
	v_add_co_u32_e32 v2, vcc, 0x1000, v2
	s_waitcnt vmcnt(3)
	v_mov_b32_e32 v143, v34
	v_addc_co_u32_e32 v3, vcc, 0, v3, vcc
	global_load_dwordx4 v[50:53], v[2:3], off nt
	global_load_dwordx4 v[54:57], v[2:3], off offset:1024 nt
	global_load_dwordx4 v[58:61], v[2:3], off offset:2048 nt
	global_load_dwordx4 v[62:65], v[2:3], off offset:3072 nt

.LBB0_37:
	s_branch .LBB0_40
	v_fma_f32 v2, v134, v143, 0
	v_fmac_f32_e32 v2, v135, v35
	v_fmac_f32_e32 v2, v136, v36
	v_fmac_f32_e32 v2, v137, v37
	s_waitcnt vmcnt(6)
	v_fmac_f32_e32 v2, v126, v38
	v_fmac_f32_e32 v2, v127, v39
	v_fmac_f32_e32 v2, v128, v40
	v_fmac_f32_e32 v2, v129, v41
	s_waitcnt vmcnt(5)
	v_fmac_f32_e32 v2, v118, v42
	v_fmac_f32_e32 v2, v119, v43
	v_fmac_f32_e32 v2, v120, v44
	v_fmac_f32_e32 v2, v121, v45
	s_waitcnt vmcnt(4)
	v_fmac_f32_e32 v2, v110, v46
	v_fmac_f32_e32 v2, v111, v47
	v_fmac_f32_e32 v2, v112, v48
	v_fmac_f32_e32 v2, v113, v49
	s_waitcnt vmcnt(3)
	v_fmac_f32_e32 v2, v114, v50
	v_fmac_f32_e32 v2, v115, v51
	v_fmac_f32_e32 v2, v116, v52
	v_fmac_f32_e32 v2, v117, v53
	s_waitcnt vmcnt(2)
	v_fmac_f32_e32 v2, v106, v54
	v_fmac_f32_e32 v2, v107, v55
	v_fmac_f32_e32 v2, v108, v56
	v_fmac_f32_e32 v2, v109, v57
	s_waitcnt vmcnt(1)
	v_fmac_f32_e32 v2, v102, v58
	v_fmac_f32_e32 v2, v103, v59
	v_fmac_f32_e32 v2, v104, v60
	v_fmac_f32_e32 v2, v105, v61
	s_waitcnt vmcnt(0)
	v_fmac_f32_e32 v2, v98, v62
	v_fmac_f32_e32 v2, v99, v63
	v_fmac_f32_e32 v2, v100, v64
	v_fmac_f32_e32 v2, v101, v65
	ds_bpermute_b32 v3, v1, v2
	s_waitcnt lgkmcnt(0)
	v_add_f32_e32 v2, v2, v3
	ds_bpermute_b32 v3, v152, v2
	s_waitcnt lgkmcnt(0)
	v_add_f32_e32 v2, v2, v3
	ds_bpermute_b32 v3, v153, v2
	s_waitcnt lgkmcnt(0)
	v_add_f32_e32 v2, v2, v3
	ds_bpermute_b32 v3, v154, v2
	s_waitcnt lgkmcnt(0)
	v_add_f32_e32 v2, v2, v3
	ds_bpermute_b32 v3, v155, v2
	s_waitcnt lgkmcnt(0)
	v_add_f32_e32 v2, v2, v3
	ds_bpermute_b32 v3, v156, v2
	s_and_saveexec_b64 s[8:9], s[10:11]
	s_cbranch_execz .LBB0_39
	v_lshl_add_u64 v[4:5], v[146:147], 2, s[12:13]
	s_waitcnt lgkmcnt(0)
	v_add_f32_e32 v2, v2, v3
	global_store_dword v[4:5], v2, off offset:8

.LBB0_40:
	v_or_b32_e32 v110, 3, v162
	v_mov_b32_e32 v111, 0
	s_waitcnt lgkmcnt(0)
	v_lshl_add_u64 v[2:3], s[20:21], 0, v[110:111]
	v_lshlrev_b64 v[2:3], 13, v[2:3]
	v_lshl_add_u64 v[2:3], s[22:23], 0, v[2:3]
	v_mov_b32_e32 v4, v142
	v_mov_b32_e32 v5, v111
	v_lshl_add_u64 v[2:3], v[2:3], 0, v[4:5]
	v_add_co_u32_e32 v6, vcc, 0x2000, v2
	s_mov_b64 s[8:9], 0x2000
	s_nop 0
	v_addc_co_u32_e32 v7, vcc, 0, v3, vcc
	v_lshl_add_u64 v[4:5], v[2:3], 0, s[8:9]
	v_add_co_u32_e32 v2, vcc, 0x3000, v2
	global_load_dwordx4 v[114:117], v[4:5], off offset:1024 nt
	global_load_dwordx4 v[106:109], v[4:5], off offset:2048 nt
	global_load_dwordx4 v[126:129], v[6:7], off nt
	global_load_dwordx4 v[98:101], v[4:5], off offset:3072 nt
	v_addc_co_u32_e32 v3, vcc, 0, v3, vcc
	global_load_dwordx4 v[102:105], v[2:3], off nt
	global_load_dwordx4 v[86:89], v[2:3], off offset:1024 nt
	global_load_dwordx4 v[78:81], v[2:3], off offset:2048 nt
	global_load_dwordx4 v[70:73], v[2:3], off offset:3072 nt
	s_and_b64 vcc, exec, s[6:7]
	s_branch .LBB0_42
	global_load_dword v2, v[148:149], off offset:12
	v_mov_b32_e32 v4, 0x7cff
	v_mov_b32_e32 v3, v111
	s_waitcnt vmcnt(0)
	v_med3_i32 v2, v2, 0, v4
	v_lshlrev_b32_e32 v2, 13, v2
	v_lshl_add_u64 v[2:3], v[144:145], 0, v[2:3]
	global_load_dwordx4 v[34:37], v[2:3], off nt
	global_load_dwordx4 v[38:41], v[2:3], off offset:1024 nt
	global_load_dwordx4 v[42:45], v[2:3], off offset:2048 nt
	global_load_dwordx4 v[46:49], v[2:3], off offset:3072 nt
	v_add_co_u32_e32 v2, vcc, 0x1000, v2
	s_waitcnt vmcnt(3)
	v_mov_b32_e32 v143, v34
	v_addc_co_u32_e32 v3, vcc, 0, v3, vcc
	global_load_dwordx4 v[50:53], v[2:3], off nt
	global_load_dwordx4 v[54:57], v[2:3], off offset:1024 nt
	global_load_dwordx4 v[58:61], v[2:3], off offset:2048 nt
	global_load_dwordx4 v[62:65], v[2:3], off offset:3072 nt

.LBB0_49:
	s_branch .LBB0_52
	v_fma_f32 v2, v138, v143, 0
	v_fmac_f32_e32 v2, v139, v35
	v_fmac_f32_e32 v2, v140, v36
	v_fmac_f32_e32 v2, v141, v37
	s_waitcnt vmcnt(6)
	v_fmac_f32_e32 v2, v130, v38
	v_fmac_f32_e32 v2, v131, v39
	v_fmac_f32_e32 v2, v132, v40
	v_fmac_f32_e32 v2, v133, v41
	s_waitcnt vmcnt(5)
	v_fmac_f32_e32 v2, v122, v42
	v_fmac_f32_e32 v2, v123, v43
	v_fmac_f32_e32 v2, v124, v44
	v_fmac_f32_e32 v2, v125, v45
	s_waitcnt vmcnt(4)
	v_fmac_f32_e32 v2, v90, v46
	v_fmac_f32_e32 v2, v91, v47
	v_fmac_f32_e32 v2, v92, v48
	v_fmac_f32_e32 v2, v93, v49
	s_waitcnt vmcnt(3)
	v_fmac_f32_e32 v2, v94, v50
	v_fmac_f32_e32 v2, v95, v51
	v_fmac_f32_e32 v2, v96, v52
	v_fmac_f32_e32 v2, v97, v53
	s_waitcnt vmcnt(2)
	v_fmac_f32_e32 v2, v82, v54
	v_fmac_f32_e32 v2, v83, v55
	v_fmac_f32_e32 v2, v84, v56
	v_fmac_f32_e32 v2, v85, v57
	s_waitcnt vmcnt(1)
	v_fmac_f32_e32 v2, v74, v58
	v_fmac_f32_e32 v2, v75, v59
	v_fmac_f32_e32 v2, v76, v60
	v_fmac_f32_e32 v2, v77, v61
	s_waitcnt vmcnt(0)
	v_fmac_f32_e32 v2, v66, v62
	v_fmac_f32_e32 v2, v67, v63
	v_fmac_f32_e32 v2, v68, v64
	v_fmac_f32_e32 v2, v69, v65
	ds_bpermute_b32 v3, v1, v2
	s_waitcnt lgkmcnt(0)
	v_add_f32_e32 v2, v2, v3
	ds_bpermute_b32 v3, v152, v2
	s_waitcnt lgkmcnt(0)
	v_add_f32_e32 v2, v2, v3
	ds_bpermute_b32 v3, v153, v2
	s_waitcnt lgkmcnt(0)
	v_add_f32_e32 v2, v2, v3
	ds_bpermute_b32 v3, v154, v2
	s_waitcnt lgkmcnt(0)
	v_add_f32_e32 v2, v2, v3
	ds_bpermute_b32 v3, v155, v2
	s_waitcnt lgkmcnt(0)
	v_add_f32_e32 v2, v2, v3
	ds_bpermute_b32 v3, v156, v2
	s_and_saveexec_b64 s[8:9], s[10:11]
	s_cbranch_execz .LBB0_51
	v_lshl_add_u64 v[4:5], v[146:147], 2, s[12:13]
	s_waitcnt lgkmcnt(0)
	v_add_f32_e32 v2, v2, v3
	global_store_dword v[4:5], v2, off offset:12

.LBB0_52:
	v_or_b32_e32 v130, 4, v162
	v_mov_b32_e32 v131, 0
	s_waitcnt lgkmcnt(0)
	v_lshl_add_u64 v[2:3], s[20:21], 0, v[130:131]
	v_lshlrev_b64 v[2:3], 13, v[2:3]
	v_lshl_add_u64 v[2:3], s[22:23], 0, v[2:3]
	v_mov_b32_e32 v4, v142
	v_mov_b32_e32 v5, v131
	v_lshl_add_u64 v[2:3], v[2:3], 0, v[4:5]
	v_add_co_u32_e32 v6, vcc, 0x2000, v2
	s_mov_b64 s[8:9], 0x2000
	s_nop 0
	v_addc_co_u32_e32 v7, vcc, 0, v3, vcc
	v_lshl_add_u64 v[4:5], v[2:3], 0, s[8:9]
	v_add_co_u32_e32 v2, vcc, 0x3000, v2
	global_load_dwordx4 v[118:121], v[4:5], off offset:1024 nt
	global_load_dwordx4 v[110:113], v[4:5], off offset:2048 nt
	global_load_dwordx4 v[122:125], v[6:7], off nt
	global_load_dwordx4 v[90:93], v[4:5], off offset:3072 nt
	v_addc_co_u32_e32 v3, vcc, 0, v3, vcc
	global_load_dwordx4 v[94:97], v[2:3], off nt
	global_load_dwordx4 v[82:85], v[2:3], off offset:1024 nt
	global_load_dwordx4 v[74:77], v[2:3], off offset:2048 nt
	global_load_dwordx4 v[66:69], v[2:3], off offset:3072 nt
	s_and_b64 vcc, exec, s[6:7]
	s_branch .LBB0_54
	global_load_dword v2, v[148:149], off offset:16
	v_mov_b32_e32 v4, 0x7cff
	v_mov_b32_e32 v3, v131
	s_waitcnt vmcnt(0)
	v_med3_i32 v2, v2, 0, v4
	v_lshlrev_b32_e32 v2, 13, v2
	v_lshl_add_u64 v[2:3], v[144:145], 0, v[2:3]
	global_load_dwordx4 v[34:37], v[2:3], off nt
	global_load_dwordx4 v[38:41], v[2:3], off offset:1024 nt
	global_load_dwordx4 v[42:45], v[2:3], off offset:2048 nt
	global_load_dwordx4 v[46:49], v[2:3], off offset:3072 nt
	v_add_co_u32_e32 v2, vcc, 0x1000, v2
	s_waitcnt vmcnt(3)
	v_mov_b32_e32 v143, v34
	v_addc_co_u32_e32 v3, vcc, 0, v3, vcc
	global_load_dwordx4 v[50:53], v[2:3], off nt
	global_load_dwordx4 v[54:57], v[2:3], off offset:1024 nt
	global_load_dwordx4 v[58:61], v[2:3], off offset:2048 nt
	global_load_dwordx4 v[62:65], v[2:3], off offset:3072 nt

.LBB0_61:
	s_branch .LBB0_64
	v_fma_f32 v2, v126, v143, 0
	v_fmac_f32_e32 v2, v127, v35
	v_fmac_f32_e32 v2, v128, v36
	v_fmac_f32_e32 v2, v129, v37
	s_waitcnt vmcnt(6)
	v_fmac_f32_e32 v2, v114, v38
	v_fmac_f32_e32 v2, v115, v39
	v_fmac_f32_e32 v2, v116, v40
	v_fmac_f32_e32 v2, v117, v41
	s_waitcnt vmcnt(5)
	v_fmac_f32_e32 v2, v106, v42
	v_fmac_f32_e32 v2, v107, v43
	v_fmac_f32_e32 v2, v108, v44
	v_fmac_f32_e32 v2, v109, v45
	s_waitcnt vmcnt(4)
	v_fmac_f32_e32 v2, v98, v46
	v_fmac_f32_e32 v2, v99, v47
	v_fmac_f32_e32 v2, v100, v48
	v_fmac_f32_e32 v2, v101, v49
	s_waitcnt vmcnt(3)
	v_fmac_f32_e32 v2, v102, v50
	v_fmac_f32_e32 v2, v103, v51
	v_fmac_f32_e32 v2, v104, v52
	v_fmac_f32_e32 v2, v105, v53
	s_waitcnt vmcnt(2)
	v_fmac_f32_e32 v2, v86, v54
	v_fmac_f32_e32 v2, v87, v55
	v_fmac_f32_e32 v2, v88, v56
	v_fmac_f32_e32 v2, v89, v57
	s_waitcnt vmcnt(1)
	v_fmac_f32_e32 v2, v78, v58
	v_fmac_f32_e32 v2, v79, v59
	v_fmac_f32_e32 v2, v80, v60
	v_fmac_f32_e32 v2, v81, v61
	s_waitcnt vmcnt(0)
	v_fmac_f32_e32 v2, v70, v62
	v_fmac_f32_e32 v2, v71, v63
	v_fmac_f32_e32 v2, v72, v64
	v_fmac_f32_e32 v2, v73, v65
	ds_bpermute_b32 v3, v1, v2
	s_waitcnt lgkmcnt(0)
	v_add_f32_e32 v2, v2, v3
	ds_bpermute_b32 v3, v152, v2
	s_waitcnt lgkmcnt(0)
	v_add_f32_e32 v2, v2, v3
	ds_bpermute_b32 v3, v153, v2
	s_waitcnt lgkmcnt(0)
	v_add_f32_e32 v2, v2, v3
	ds_bpermute_b32 v3, v154, v2
	s_waitcnt lgkmcnt(0)
	v_add_f32_e32 v2, v2, v3
	ds_bpermute_b32 v3, v155, v2
	s_waitcnt lgkmcnt(0)
	v_add_f32_e32 v2, v2, v3
	ds_bpermute_b32 v3, v156, v2
	s_and_saveexec_b64 s[8:9], s[10:11]
	s_cbranch_execz .LBB0_63
	v_lshl_add_u64 v[4:5], v[146:147], 2, s[12:13]
	s_waitcnt lgkmcnt(0)
	v_add_f32_e32 v2, v2, v3
	global_store_dword v[4:5], v2, off offset:16

.LBB0_64:
	v_or_b32_e32 v130, 5, v162
	v_mov_b32_e32 v131, 0
	s_waitcnt lgkmcnt(0)
	v_lshl_add_u64 v[2:3], s[20:21], 0, v[130:131]
	v_lshlrev_b64 v[2:3], 13, v[2:3]
	v_lshl_add_u64 v[2:3], s[22:23], 0, v[2:3]
	v_mov_b32_e32 v4, v142
	v_mov_b32_e32 v5, v131
	v_lshl_add_u64 v[2:3], v[2:3], 0, v[4:5]
	v_add_co_u32_e32 v6, vcc, 0x2000, v2
	s_mov_b64 s[8:9], 0x2000
	s_nop 0
	v_addc_co_u32_e32 v7, vcc, 0, v3, vcc
	v_lshl_add_u64 v[4:5], v[2:3], 0, s[8:9]
	v_add_co_u32_e32 v2, vcc, 0x3000, v2
	global_load_dwordx4 v[114:117], v[4:5], off offset:1024 nt
	global_load_dwordx4 v[106:109], v[4:5], off offset:2048 nt
	global_load_dwordx4 v[126:129], v[6:7], off nt
	global_load_dwordx4 v[98:101], v[4:5], off offset:3072 nt
	v_addc_co_u32_e32 v3, vcc, 0, v3, vcc
	global_load_dwordx4 v[102:105], v[2:3], off nt
	global_load_dwordx4 v[86:89], v[2:3], off offset:1024 nt
	global_load_dwordx4 v[78:81], v[2:3], off offset:2048 nt
	global_load_dwordx4 v[70:73], v[2:3], off offset:3072 nt
	s_and_b64 vcc, exec, s[6:7]
	s_branch .LBB0_66
	global_load_dword v2, v[148:149], off offset:20
	v_mov_b32_e32 v4, 0x7cff
	v_mov_b32_e32 v3, v131
	s_waitcnt vmcnt(0)
	v_med3_i32 v2, v2, 0, v4
	v_lshlrev_b32_e32 v2, 13, v2
	v_lshl_add_u64 v[2:3], v[144:145], 0, v[2:3]
	global_load_dwordx4 v[34:37], v[2:3], off nt
	global_load_dwordx4 v[38:41], v[2:3], off offset:1024 nt
	global_load_dwordx4 v[42:45], v[2:3], off offset:2048 nt
	global_load_dwordx4 v[46:49], v[2:3], off offset:3072 nt
	v_add_co_u32_e32 v2, vcc, 0x1000, v2
	s_waitcnt vmcnt(3)
	v_mov_b32_e32 v143, v34
	v_addc_co_u32_e32 v3, vcc, 0, v3, vcc
	global_load_dwordx4 v[50:53], v[2:3], off nt
	global_load_dwordx4 v[54:57], v[2:3], off offset:1024 nt
	global_load_dwordx4 v[58:61], v[2:3], off offset:2048 nt
	global_load_dwordx4 v[62:65], v[2:3], off offset:3072 nt

.LBB0_73:
	s_branch .LBB0_76
	v_fma_f32 v2, v122, v143, 0
	v_fmac_f32_e32 v2, v123, v35
	v_fmac_f32_e32 v2, v124, v36
	v_fmac_f32_e32 v2, v125, v37
	s_waitcnt vmcnt(6)
	v_fmac_f32_e32 v2, v118, v38
	v_fmac_f32_e32 v2, v119, v39
	v_fmac_f32_e32 v2, v120, v40
	v_fmac_f32_e32 v2, v121, v41
	s_waitcnt vmcnt(5)
	v_fmac_f32_e32 v2, v110, v42
	v_fmac_f32_e32 v2, v111, v43
	v_fmac_f32_e32 v2, v112, v44
	v_fmac_f32_e32 v2, v113, v45
	s_waitcnt vmcnt(4)
	v_fmac_f32_e32 v2, v90, v46
	v_fmac_f32_e32 v2, v91, v47
	v_fmac_f32_e32 v2, v92, v48
	v_fmac_f32_e32 v2, v93, v49
	s_waitcnt vmcnt(3)
	v_fmac_f32_e32 v2, v94, v50
	v_fmac_f32_e32 v2, v95, v51
	v_fmac_f32_e32 v2, v96, v52
	v_fmac_f32_e32 v2, v97, v53
	s_waitcnt vmcnt(2)
	v_fmac_f32_e32 v2, v82, v54
	v_fmac_f32_e32 v2, v83, v55
	v_fmac_f32_e32 v2, v84, v56
	v_fmac_f32_e32 v2, v85, v57
	s_waitcnt vmcnt(1)
	v_fmac_f32_e32 v2, v74, v58
	v_fmac_f32_e32 v2, v75, v59
	v_fmac_f32_e32 v2, v76, v60
	v_fmac_f32_e32 v2, v77, v61
	s_waitcnt vmcnt(0)
	v_fmac_f32_e32 v2, v66, v62
	v_fmac_f32_e32 v2, v67, v63
	v_fmac_f32_e32 v2, v68, v64
	v_fmac_f32_e32 v2, v69, v65
	ds_bpermute_b32 v3, v1, v2
	s_waitcnt lgkmcnt(0)
	v_add_f32_e32 v2, v2, v3
	ds_bpermute_b32 v3, v152, v2
	s_waitcnt lgkmcnt(0)
	v_add_f32_e32 v2, v2, v3
	ds_bpermute_b32 v3, v153, v2
	s_waitcnt lgkmcnt(0)
	v_add_f32_e32 v2, v2, v3
	ds_bpermute_b32 v3, v154, v2
	s_waitcnt lgkmcnt(0)
	v_add_f32_e32 v2, v2, v3
	ds_bpermute_b32 v3, v155, v2
	s_waitcnt lgkmcnt(0)
	v_add_f32_e32 v2, v2, v3
	ds_bpermute_b32 v3, v156, v2
	s_and_saveexec_b64 s[8:9], s[10:11]
	s_cbranch_execz .LBB0_75
	v_lshl_add_u64 v[4:5], v[146:147], 2, s[12:13]
	s_waitcnt lgkmcnt(0)
	v_add_f32_e32 v2, v2, v3
	global_store_dword v[4:5], v2, off offset:20

.LBB0_76:
	v_or_b32_e32 v130, 6, v162
	v_mov_b32_e32 v131, 0
	s_waitcnt lgkmcnt(0)
	v_lshl_add_u64 v[2:3], s[20:21], 0, v[130:131]
	v_lshlrev_b64 v[2:3], 13, v[2:3]
	v_lshl_add_u64 v[2:3], s[22:23], 0, v[2:3]
	v_mov_b32_e32 v4, v142
	v_mov_b32_e32 v5, v131
	v_lshl_add_u64 v[2:3], v[2:3], 0, v[4:5]
	v_add_co_u32_e32 v6, vcc, 0x2000, v2
	s_mov_b64 s[8:9], 0x2000
	s_nop 0
	v_addc_co_u32_e32 v7, vcc, 0, v3, vcc
	v_lshl_add_u64 v[4:5], v[2:3], 0, s[8:9]
	v_add_co_u32_e32 v2, vcc, 0x3000, v2
	global_load_dwordx4 v[118:121], v[4:5], off offset:1024 nt
	global_load_dwordx4 v[110:113], v[4:5], off offset:2048 nt
	global_load_dwordx4 v[122:125], v[6:7], off nt
	global_load_dwordx4 v[90:93], v[4:5], off offset:3072 nt
	v_addc_co_u32_e32 v3, vcc, 0, v3, vcc
	global_load_dwordx4 v[94:97], v[2:3], off nt
	global_load_dwordx4 v[82:85], v[2:3], off offset:1024 nt
	global_load_dwordx4 v[74:77], v[2:3], off offset:2048 nt
	global_load_dwordx4 v[66:69], v[2:3], off offset:3072 nt
	s_and_b64 vcc, exec, s[6:7]
	s_branch .LBB0_78
	global_load_dword v2, v[148:149], off offset:24
	v_mov_b32_e32 v4, 0x7cff
	v_mov_b32_e32 v3, v131
	s_waitcnt vmcnt(0)
	v_med3_i32 v2, v2, 0, v4
	v_lshlrev_b32_e32 v2, 13, v2
	v_lshl_add_u64 v[2:3], v[144:145], 0, v[2:3]
	global_load_dwordx4 v[34:37], v[2:3], off nt
	global_load_dwordx4 v[38:41], v[2:3], off offset:1024 nt
	global_load_dwordx4 v[42:45], v[2:3], off offset:2048 nt
	global_load_dwordx4 v[46:49], v[2:3], off offset:3072 nt
	v_add_co_u32_e32 v2, vcc, 0x1000, v2
	s_waitcnt vmcnt(3)
	v_mov_b32_e32 v143, v34
	v_addc_co_u32_e32 v3, vcc, 0, v3, vcc
	global_load_dwordx4 v[50:53], v[2:3], off nt
	global_load_dwordx4 v[54:57], v[2:3], off offset:1024 nt
	global_load_dwordx4 v[58:61], v[2:3], off offset:2048 nt
	global_load_dwordx4 v[62:65], v[2:3], off offset:3072 nt

.LBB0_85:
	s_branch .LBB0_88
	v_fma_f32 v2, v126, v143, 0
	v_fmac_f32_e32 v2, v127, v35
	v_fmac_f32_e32 v2, v128, v36
	v_fmac_f32_e32 v2, v129, v37
	s_waitcnt vmcnt(6)
	v_fmac_f32_e32 v2, v114, v38
	v_fmac_f32_e32 v2, v115, v39
	v_fmac_f32_e32 v2, v116, v40
	v_fmac_f32_e32 v2, v117, v41
	s_waitcnt vmcnt(5)
	v_fmac_f32_e32 v2, v106, v42
	v_fmac_f32_e32 v2, v107, v43
	v_fmac_f32_e32 v2, v108, v44
	v_fmac_f32_e32 v2, v109, v45
	s_waitcnt vmcnt(4)
	v_fmac_f32_e32 v2, v98, v46
	v_fmac_f32_e32 v2, v99, v47
	v_fmac_f32_e32 v2, v100, v48
	v_fmac_f32_e32 v2, v101, v49
	s_waitcnt vmcnt(3)
	v_fmac_f32_e32 v2, v102, v50
	v_fmac_f32_e32 v2, v103, v51
	v_fmac_f32_e32 v2, v104, v52
	v_fmac_f32_e32 v2, v105, v53
	s_waitcnt vmcnt(2)
	v_fmac_f32_e32 v2, v86, v54
	v_fmac_f32_e32 v2, v87, v55
	v_fmac_f32_e32 v2, v88, v56
	v_fmac_f32_e32 v2, v89, v57
	s_waitcnt vmcnt(1)
	v_fmac_f32_e32 v2, v78, v58
	v_fmac_f32_e32 v2, v79, v59
	v_fmac_f32_e32 v2, v80, v60
	v_fmac_f32_e32 v2, v81, v61
	s_waitcnt vmcnt(0)
	v_fmac_f32_e32 v2, v70, v62
	v_fmac_f32_e32 v2, v71, v63
	v_fmac_f32_e32 v2, v72, v64
	v_fmac_f32_e32 v2, v73, v65
	ds_bpermute_b32 v3, v1, v2
	s_waitcnt lgkmcnt(0)
	v_add_f32_e32 v2, v2, v3
	ds_bpermute_b32 v3, v152, v2
	s_waitcnt lgkmcnt(0)
	v_add_f32_e32 v2, v2, v3
	ds_bpermute_b32 v3, v153, v2
	s_waitcnt lgkmcnt(0)
	v_add_f32_e32 v2, v2, v3
	ds_bpermute_b32 v3, v154, v2
	s_waitcnt lgkmcnt(0)
	v_add_f32_e32 v2, v2, v3
	ds_bpermute_b32 v3, v155, v2
	s_waitcnt lgkmcnt(0)
	v_add_f32_e32 v2, v2, v3
	ds_bpermute_b32 v3, v156, v2
	s_and_saveexec_b64 s[8:9], s[10:11]
	s_cbranch_execz .LBB0_87
	v_lshl_add_u64 v[4:5], v[146:147], 2, s[12:13]
	s_waitcnt lgkmcnt(0)
	v_add_f32_e32 v2, v2, v3
	global_store_dword v[4:5], v2, off offset:24

.LBB0_88:
	v_or_b32_e32 v72, 7, v157
	v_mov_b32_e32 v73, 0
	s_and_b64 vcc, exec, s[6:7]
	v_lshl_add_u64 v[70:71], s[20:21], 0, v[72:73]
	s_branch .LBB0_90
	s_waitcnt lgkmcnt(0)
	v_lshl_add_u64 v[2:3], v[70:71], 2, s[18:19]
	global_load_dword v2, v[2:3], off
	v_mov_b32_e32 v4, 0x7cff
	v_mov_b32_e32 v3, v73
	s_waitcnt vmcnt(0)
	v_med3_i32 v2, v2, 0, v4
	v_lshlrev_b32_e32 v2, 13, v2
	v_lshl_add_u64 v[2:3], v[144:145], 0, v[2:3]
	global_load_dwordx4 v[34:37], v[2:3], off nt
	global_load_dwordx4 v[38:41], v[2:3], off offset:1024 nt
	global_load_dwordx4 v[42:45], v[2:3], off offset:2048 nt
	global_load_dwordx4 v[46:49], v[2:3], off offset:3072 nt
	v_add_co_u32_e32 v2, vcc, 0x1000, v2
	s_waitcnt vmcnt(3)
	v_mov_b32_e32 v143, v34
	v_addc_co_u32_e32 v3, vcc, 0, v3, vcc
	global_load_dwordx4 v[50:53], v[2:3], off nt
	global_load_dwordx4 v[54:57], v[2:3], off offset:1024 nt
	global_load_dwordx4 v[58:61], v[2:3], off offset:2048 nt
	global_load_dwordx4 v[62:65], v[2:3], off offset:3072 nt

.LBB0_97:
	s_branch .LBB0_100
	v_fma_f32 v2, v122, v143, 0
	v_fmac_f32_e32 v2, v123, v35
	v_fmac_f32_e32 v2, v124, v36
	v_fmac_f32_e32 v2, v125, v37
	v_fmac_f32_e32 v2, v118, v38
	v_fmac_f32_e32 v2, v119, v39
	v_fmac_f32_e32 v2, v120, v40
	v_fmac_f32_e32 v2, v121, v41
	v_fmac_f32_e32 v2, v110, v42
	v_fmac_f32_e32 v2, v111, v43
	v_fmac_f32_e32 v2, v112, v44
	v_fmac_f32_e32 v2, v113, v45
	v_fmac_f32_e32 v2, v90, v46
	v_fmac_f32_e32 v2, v91, v47
	v_fmac_f32_e32 v2, v92, v48
	v_fmac_f32_e32 v2, v93, v49
	v_fmac_f32_e32 v2, v94, v50
	v_fmac_f32_e32 v2, v95, v51
	v_fmac_f32_e32 v2, v96, v52
	v_fmac_f32_e32 v2, v97, v53
	v_fmac_f32_e32 v2, v82, v54
	v_fmac_f32_e32 v2, v83, v55
	v_fmac_f32_e32 v2, v84, v56
	v_fmac_f32_e32 v2, v85, v57
	v_fmac_f32_e32 v2, v74, v58
	v_fmac_f32_e32 v2, v75, v59
	v_fmac_f32_e32 v2, v76, v60
	v_fmac_f32_e32 v2, v77, v61
	v_fmac_f32_e32 v2, v66, v62
	v_fmac_f32_e32 v2, v67, v63
	v_fmac_f32_e32 v2, v68, v64
	v_fmac_f32_e32 v2, v69, v65
	ds_bpermute_b32 v1, v1, v2
	s_waitcnt lgkmcnt(0)
	v_add_f32_e32 v1, v2, v1
	ds_bpermute_b32 v2, v152, v1
	s_waitcnt lgkmcnt(0)
	v_add_f32_e32 v1, v1, v2
	ds_bpermute_b32 v2, v153, v1
	s_waitcnt lgkmcnt(0)
	v_add_f32_e32 v1, v1, v2
	ds_bpermute_b32 v2, v154, v1
	s_waitcnt lgkmcnt(0)
	v_add_f32_e32 v1, v1, v2
	ds_bpermute_b32 v2, v155, v1
	s_waitcnt lgkmcnt(0)
	v_add_f32_e32 v1, v1, v2
	ds_bpermute_b32 v2, v156, v1
	s_and_saveexec_b64 s[4:5], s[10:11]
	s_cbranch_execz .LBB0_99
	v_lshl_add_u64 v[4:5], v[70:71], 2, s[12:13]
	s_waitcnt lgkmcnt(0)
	v_add_f32_e32 v1, v1, v2
	global_store_dword v[4:5], v1, off

_Z15gemm_lse_kernelPKhS0_PKjS2_PfPiP15HIP_vector_typeIfLj2EE:
	s_load_dwordx2 s[60:61], s[0:1], 0x30
	s_load_dwordx2 s[62:63], s[0:1], 0x20
	s_mov_b32 s59, s2
	v_readfirstlane_b32 s28, v0
	s_mov_b32 s58, s28
	s_bfe_u32 s33, s28, 0x20006
	s_and_b32 s3, s2, 7
	v_and_b32_e32 v184, 63, v0
	s_ashr_i32 s19, s2, 3
	s_mul_i32 s18, s33, 0xc00
	s_mul_i32 s20, s3, 0xfa
	v_lshl_or_b32 v1, v184, 3, s18
	s_add_i32 s20, s20, s19
	v_add_u32_e32 v198, 0x2400, v1
	v_add_u32_e32 v199, 0x2a00, v1
	s_cmpk_gt_i32 s20, 0x7bf
	s_cbranch_scc0 .LBB1_2
	s_add_i32 s26, s20, 0xfffff840
	s_load_dwordx2 s[16:17], s[0:1], 0x18
	s_movk_i32 s9, 0x7c
	s_cbranch_execz .LBB1_3
	s_branch .LBB1_4

.LBB1_12:
	s_lshr_b32 s31, s28, 8
	v_lshl_or_b32 v201, s31, 12, v200
	s_barrier
	ds_read_b128 v[152:155], v201 offset:3072
	ds_read_b128 v[156:159], v201 offset:2048
	ds_read_b128 v[160:163], v201 offset:1024
	ds_read_b128 v[164:167], v201
	v_add_u32_e32 v1, s18, v200
	ds_read_b64 v[132:133], v199
	ds_read_b64 v[138:139], v198
	ds_read_b128 v[128:131], v1 offset:9728
	ds_read_b128 v[134:137], v1 offset:8192
	s_load_dwordx2 s[14:15], s[0:1], 0x20
	s_add_i32 s0, s18, 0x2000
	s_cmp_lt_i32 s19, 26
	s_cselect_b32 s24, 8, 7
	v_or_b32_e32 v202, s0, v200
	s_and_b32 s25, s20, 7
	s_mov_b64 s[18:19], -1
	s_and_b64 vcc, exec, s[2:3]
	v_and_b32_e32 v205, 31, v0
	v_cmp_gt_u32_e64 s[0:1], 32, v184
	v_or_b32_e32 v203, 32, v184
	v_mbcnt_lo_u32_b32 v204, -1, 0
	s_cbranch_vccz .LBB1_26
	s_waitcnt lgkmcnt(0)
	s_load_dwordx4 s[64:67], s[60:61], 0x40
	s_load_dwordx2 s[68:69], s[60:61], 0x50
	s_lshl_b32 s72, s59, 4
	s_lshr_b32 s73, s58, 6
	s_lshl_b32 s73, s73, 1
	s_add_u32 s72, s72, s73
	s_lshl_b32 s73, s72, 2
	s_sub_u32 s62, s62, 0x4000
	s_subb_u32 s63, s63, 0
	s_add_u32 s62, s62, s73
	s_addc_u32 s63, s63, 0
	s_waitcnt lgkmcnt(0)
	s_add_u32 s68, s68, s73
	s_addc_u32 s69, s69, 0
	s_load_dwordx2 s[76:77], s[68:69], 0x0
	v_mbcnt_lo_u32_b32 v245, -1, 0
	v_mbcnt_hi_u32_b32 v245, -1, v245
	v_lshlrev_b32_e32 v245, 4, v245
	v_mov_b32_e32 v244, 0
	s_waitcnt lgkmcnt(0)
	s_max_i32 s75, s76, 0
	s_min_i32 s75, s75, 0x7cff
	s_lshl_b32 s82, s75, 13
	s_add_u32 s84, s66, s82
	s_addc_u32 s85, s67, 0
	s_lshl_b32 s82, s72, 13
	s_add_u32 s86, s64, s82
	s_addc_u32 s87, s65, 0
	global_load_dwordx4 v[228:231], v245, s[84:85] nt
	global_load_dwordx4 v[232:235], v245, s[84:85] offset:1024 nt
	global_load_dwordx4 v[236:239], v245, s[86:87] nt
	global_load_dwordx4 v[240:243], v245, s[86:87] offset:1024 nt
	s_add_u32 s84, s84, 0x800
	s_addc_u32 s85, s85, 0
	s_add_u32 s86, s86, 0x800
	s_addc_u32 s87, s87, 0
	s_mov_b32 s74, 1
	s_lshl_b32 s30, s33, 8
	v_lshlrev_b32_e32 v206, 2, v205
	v_or_b32_e32 v0, s30, v206
	v_or_b32_e32 v1, 0x1e400, v0
	v_or_b32_e32 v0, 0x1e480, v0
	s_lshl_b32 s31, s31, 9
	ds_read_b32 v195, v0
	ds_read_b32 v194, v1
	v_or_b32_e32 v0, s31, v206
	v_add_u32_e32 v0, 0x1e000, v0
	s_and_b32 s2, s28, 0xffffffc0
	ds_read2_b32 v[192:193], v0 offset0:64 offset1:96
	ds_read2_b32 v[196:197], v0 offset1:32
	s_mov_b32 s3, 0
	s_addk_i32 s2, 0xff00
	s_lshl_b64 s[18:19], s[2:3], 2
	s_add_u32 s16, s16, s18
	v_mov_b32_e32 v187, 0
	s_addc_u32 s17, s17, s19
	s_waitcnt lgkmcnt(0)
	v_mov_b64_e32 v[0:1], v[128:129]
	v_mov_b64_e32 v[6:7], v[134:135]
	v_mov_b64_e32 v[12:13], v[152:153]
	v_mov_b64_e32 v[16:17], v[156:157]
	v_mov_b64_e32 v[20:21], v[160:161]
	v_mov_b64_e32 v[24:25], v[164:165]
	v_lshl_add_u64 v[188:189], s[14:15], 0, v[186:187]
	v_lshl_add_u64 v[190:191], s[16:17], 0, v[186:187]
	s_lshl_b32 s33, s33, 6
	v_mov_b32_e32 v185, v187
	s_mov_b32 s17, 1
	v_mbcnt_hi_u32_b32 v187, -1, v204
	s_mov_b32 s34, 0x71800000
	s_mov_b32 s35, 0xd800000
	v_mov_b32_e32 v207, 1
	s_movk_i32 s36, 0x7d0
	v_mov_b32_e32 v208, v199
	v_mov_b32_e32 v209, v198
	s_mov_b32 s37, s26
	v_mov_b32_e32 v210, v200
	v_mov_b32_e32 v211, v201
	v_mov_b32_e32 v212, v202
	v_mov_b64_e32 v[4:5], v[132:133]
	v_mov_b64_e32 v[10:11], v[138:139]
	v_mov_b64_e32 v[2:3], v[130:131]
	v_mov_b64_e32 v[8:9], v[136:137]
	v_mov_b64_e32 v[14:15], v[154:155]
	v_mov_b64_e32 v[18:19], v[158:159]
	v_mov_b64_e32 v[22:23], v[162:163]
	v_mov_b64_e32 v[26:27], v[166:167]
	s_mov_b32 s38, 0
	s_branch .LBB1_15

.LBB1_15:
	s_waitcnt vmcnt(10)
	s_mul_i32 s18, s17, 0x5000
	s_waitcnt lgkmcnt(0)
	s_barrier
	v_add_u32_e32 v64, s18, v212
	v_add_u32_e32 v65, s18, v209
	ds_read_b128 v[168:171], v64
	ds_read_b128 v[214:217], v64 offset:1536
	v_add_u32_e32 v64, s18, v208
	s_waitcnt lgkmcnt(0)
	v_mfma_scale_f32_32x32x64_f8f6f4 v[112:127], v[24:27], v[6:11], 0, v196, v194 op_sel_hi:[0,0,0] cbsz:4 blgp:2
	ds_read_b64 v[172:173], v65
	ds_read_b64 v[218:219], v64
	v_add_u32_e32 v174, s18, v211
	ds_read_b128 v[140:143], v174
	ds_read_b128 v[144:147], v174 offset:1024
	ds_read_b128 v[148:151], v174 offset:2048
	ds_read_b128 v[220:223], v174 offset:3072
	s_add_i32 s18, s17, 1
	s_cmp_lg_u32 s17, 5
	s_mov_b32 s2, s38
	s_mov_b32 s16, s37
	v_mfma_scale_f32_32x32x64_f8f6f4 v[48:63], v[24:27], v[0:5], 0, v196, v195 op_sel_hi:[0,0,0] cbsz:4 blgp:2
	s_cselect_b32 s17, s18, 0
	v_mfma_scale_f32_32x32x64_f8f6f4 v[96:111], v[20:23], v[6:11], 0, v197, v194 op_sel_hi:[0,0,0] cbsz:4 blgp:2
	v_mfma_scale_f32_32x32x64_f8f6f4 v[32:47], v[20:23], v[0:5], 0, v197, v195 op_sel_hi:[0,0,0] cbsz:4 blgp:2
	v_mfma_scale_f32_32x32x64_f8f6f4 v[80:95], v[16:19], v[6:11], 0, v192, v194 op_sel_hi:[0,0,0] cbsz:4 blgp:2
	v_mfma_scale_f32_32x32x64_f8f6f4 v[16:31], v[16:19], v[0:5], 0, v192, v195 op_sel_hi:[0,0,0] cbsz:4 blgp:2
	v_mfma_scale_f32_32x32x64_f8f6f4 v[64:79], v[12:15], v[6:11], 0, v193, v194 op_sel_hi:[0,0,0] cbsz:4 blgp:2
	v_mfma_scale_f32_32x32x64_f8f6f4 v[0:15], v[12:15], v[0:5], 0, v193, v195 op_sel_hi:[0,0,0] cbsz:4 blgp:2
	s_waitcnt vmcnt(15)
	s_mul_i32 s18, s17, 0x5000
	s_waitcnt lgkmcnt(0)
	v_mfma_scale_f32_32x32x64_f8f6f4 v[112:127], v[140:143], v[168:173], v[112:127], v196, v194 op_sel_hi:[0,0,0] cbsz:4 blgp:2
	v_add_u32_e32 v213, s18, v211
	v_mfma_scale_f32_32x32x64_f8f6f4 v[48:63], v[140:143], v[214:219], v[48:63], v196, v195 op_sel_hi:[0,0,0] cbsz:4 blgp:2
	v_add_u32_e32 v140, s18, v212
	v_mfma_scale_f32_32x32x64_f8f6f4 v[96:111], v[144:147], v[168:173], v[96:111], v197, v194 op_sel_hi:[0,0,0] cbsz:4 blgp:2
	v_mfma_scale_f32_32x32x64_f8f6f4 v[32:47], v[144:147], v[214:219], v[32:47], v197, v195 op_sel_hi:[0,0,0] cbsz:4 blgp:2
	v_add_u32_e32 v144, s18, v209
	v_add_u32_e32 v145, s18, v208
	s_add_i32 s18, s17, 1
	s_cmp_lg_u32 s17, 5
	s_cselect_b32 s17, s18, 0
	v_mfma_scale_f32_32x32x64_f8f6f4 v[80:95], v[148:151], v[168:173], v[80:95], v192, v194 op_sel_hi:[0,0,0] cbsz:4 blgp:2
	v_mfma_scale_f32_32x32x64_f8f6f4 v[16:31], v[148:151], v[214:219], v[16:31], v192, v195 op_sel_hi:[0,0,0] cbsz:4 blgp:2
	ds_read_b128 v[146:149], v140
	ds_read_b128 v[140:143], v140 offset:1536
	ds_read_b64 v[150:151], v144
	ds_read_b64 v[144:145], v145
	v_mfma_scale_f32_32x32x64_f8f6f4 v[64:79], v[220:223], v[168:173], v[64:79], v193, v194 op_sel_hi:[0,0,0] cbsz:4 blgp:2
	ds_read_b128 v[180:183], v213
	ds_read_b128 v[176:179], v213 offset:1024
	ds_read_b128 v[172:175], v213 offset:2048
	ds_read_b128 v[168:171], v213 offset:3072
	v_mfma_scale_f32_32x32x64_f8f6f4 v[0:15], v[220:223], v[214:219], v[0:15], v193, v195 op_sel_hi:[0,0,0] cbsz:4 blgp:2
	s_mov_b32 s18, 0
.LBB1_16:
	s_waitcnt vmcnt(10)
	s_mul_i32 s19, s17, 0x5000
	s_waitcnt lgkmcnt(0)
	v_mfma_scale_f32_32x32x64_f8f6f4 v[112:127], v[180:183], v[146:151], v[112:127], v196, v194 op_sel_hi:[0,0,0] cbsz:4 blgp:2
	s_barrier
	v_mfma_scale_f32_32x32x64_f8f6f4 v[48:63], v[180:183], v[140:145], v[48:63], v196, v195 op_sel_hi:[0,0,0] cbsz:4 blgp:2
	v_add_u32_e32 v182, s19, v211
	v_mfma_scale_f32_32x32x64_f8f6f4 v[96:111], v[176:179], v[146:151], v[96:111], v197, v194 op_sel_hi:[0,0,0] cbsz:4 blgp:2
	v_mfma_scale_f32_32x32x64_f8f6f4 v[32:47], v[176:179], v[140:145], v[32:47], v197, v195 op_sel_hi:[0,0,0] cbsz:4 blgp:2
	v_add_u32_e32 v176, s19, v212
	v_add_u32_e32 v177, s19, v209
	v_add_u32_e32 v178, s19, v208
	s_add_i32 s19, s17, 1
	s_cmp_lg_u32 s17, 5
	s_cselect_b32 s17, s19, 0
	v_mfma_scale_f32_32x32x64_f8f6f4 v[80:95], v[172:175], v[146:151], v[80:95], v192, v194 op_sel_hi:[0,0,0] cbsz:4 blgp:2
	v_mfma_scale_f32_32x32x64_f8f6f4 v[16:31], v[172:175], v[140:145], v[16:31], v192, v195 op_sel_hi:[0,0,0] cbsz:4 blgp:2
	ds_read_b128 v[172:175], v176
	ds_read_b128 v[214:217], v176 offset:1536
	ds_read_b64 v[176:177], v177
	ds_read_b64 v[218:219], v178
	v_mfma_scale_f32_32x32x64_f8f6f4 v[64:79], v[168:171], v[146:151], v[64:79], v193, v194 op_sel_hi:[0,0,0] cbsz:4 blgp:2
	ds_read_b128 v[146:149], v182
	ds_read_b128 v[178:181], v182 offset:1024
	ds_read_b128 v[220:223], v182 offset:2048
	ds_read_b128 v[224:227], v182 offset:3072
	v_mfma_scale_f32_32x32x64_f8f6f4 v[0:15], v[168:171], v[140:145], v[0:15], v193, v195 op_sel_hi:[0,0,0] cbsz:4 blgp:2
	s_waitcnt vmcnt(15)
	s_mul_i32 s19, s17, 0x5000
	s_waitcnt lgkmcnt(0)
	v_mfma_scale_f32_32x32x64_f8f6f4 v[112:127], v[146:149], v[172:177], v[112:127], v196, v194 op_sel_hi:[0,0,0] cbsz:4 blgp:2
	v_add_u32_e32 v140, s19, v212
	v_add_u32_e32 v144, s19, v209
	v_add_u32_e32 v145, s19, v208
	v_add_u32_e32 v168, s19, v211
	v_mfma_scale_f32_32x32x64_f8f6f4 v[48:63], v[146:149], v[214:219], v[48:63], v196, v195 op_sel_hi:[0,0,0] cbsz:4 blgp:2
	ds_read_b128 v[146:149], v140
	ds_read_b128 v[140:143], v140 offset:1536
	ds_read_b64 v[150:151], v144
	ds_read_b64 v[144:145], v145
	s_add_i32 s19, s17, 1
	s_cmp_lg_u32 s17, 5
	s_cselect_b32 s17, s19, 0
	v_mfma_scale_f32_32x32x64_f8f6f4 v[96:111], v[178:181], v[172:177], v[96:111], v197, v194 op_sel_hi:[0,0,0] cbsz:4 blgp:2
	v_mfma_scale_f32_32x32x64_f8f6f4 v[32:47], v[178:181], v[214:219], v[32:47], v197, v195 op_sel_hi:[0,0,0] cbsz:4 blgp:2
	v_mfma_scale_f32_32x32x64_f8f6f4 v[80:95], v[220:223], v[172:177], v[80:95], v192, v194 op_sel_hi:[0,0,0] cbsz:4 blgp:2
	v_mfma_scale_f32_32x32x64_f8f6f4 v[16:31], v[220:223], v[214:219], v[16:31], v192, v195 op_sel_hi:[0,0,0] cbsz:4 blgp:2
	v_mfma_scale_f32_32x32x64_f8f6f4 v[64:79], v[224:227], v[172:177], v[64:79], v193, v194 op_sel_hi:[0,0,0] cbsz:4 blgp:2
	ds_read_b128 v[180:183], v168
	ds_read_b128 v[176:179], v168 offset:1024
	ds_read_b128 v[172:175], v168 offset:2048
	ds_read_b128 v[168:171], v168 offset:3072
	v_mfma_scale_f32_32x32x64_f8f6f4 v[0:15], v[224:227], v[214:219], v[0:15], v193, v195 op_sel_hi:[0,0,0] cbsz:4 blgp:2
	s_add_i32 s18, s18, 2
	s_cmp_gt_u32 s18, 23
	s_cbranch_scc0 .LBB1_16
	s_add_i32 s38, s2, 1
	s_cmp_lt_u32 s38, s24
	s_cselect_b32 s2, s38, s2
	s_lshl_b32 s2, s2, 5
	s_add_i32 s2, s2, s20
	s_lshr_b32 s18, s2, 2
	s_and_b32 s18, s18, 8
	s_add_i32 s19, s2, 0xfffff840
	s_or_b32 s18, s18, s25
	s_cmpk_lt_i32 s2, 0x7c0
	s_waitcnt vmcnt(10)
	s_mul_i32 s2, s17, 0x5000
	s_waitcnt lgkmcnt(0)
	v_mfma_scale_f32_32x32x64_f8f6f4 v[112:127], v[180:183], v[146:151], v[112:127], v196, v194 op_sel_hi:[0,0,0] cbsz:4 blgp:2
	s_barrier
	v_add_u32_e32 v213, s2, v211
	s_cselect_b32 s37, s18, s19
	v_mfma_scale_f32_32x32x64_f8f6f4 v[48:63], v[180:183], v[140:145], v[48:63], v196, v195 op_sel_hi:[0,0,0] cbsz:4 blgp:2
	v_add_u32_e32 v182, s2, v208
	v_mfma_scale_f32_32x32x64_f8f6f4 v[96:111], v[176:179], v[146:151], v[96:111], v197, v194 op_sel_hi:[0,0,0] cbsz:4 blgp:2
	v_mfma_scale_f32_32x32x64_f8f6f4 v[32:47], v[176:179], v[140:145], v[32:47], v197, v195 op_sel_hi:[0,0,0] cbsz:4 blgp:2
	v_add_u32_e32 v176, s2, v212
	v_add_u32_e32 v177, s2, v209
	s_add_i32 s2, s17, 1
	s_cmp_lg_u32 s17, 5
	s_cselect_b32 s17, s2, 0
	v_mfma_scale_f32_32x32x64_f8f6f4 v[80:95], v[172:175], v[146:151], v[80:95], v192, v194 op_sel_hi:[0,0,0] cbsz:4 blgp:2
	v_mfma_scale_f32_32x32x64_f8f6f4 v[16:31], v[172:175], v[140:145], v[16:31], v192, v195 op_sel_hi:[0,0,0] cbsz:4 blgp:2
	ds_read_b128 v[172:175], v176
	ds_read_b128 v[178:181], v176 offset:1536
	ds_read_b64 v[176:177], v177
	ds_read_b64 v[182:183], v182
	v_mfma_scale_f32_32x32x64_f8f6f4 v[64:79], v[168:171], v[146:151], v[64:79], v193, v194 op_sel_hi:[0,0,0] cbsz:4 blgp:2
	ds_read_b128 v[146:149], v213
	ds_read_b128 v[214:217], v213 offset:1024
	ds_read_b128 v[218:221], v213 offset:2048
	ds_read_b128 v[222:225], v213 offset:3072
	v_mfma_scale_f32_32x32x64_f8f6f4 v[0:15], v[168:171], v[140:145], v[0:15], v193, v195 op_sel_hi:[0,0,0] cbsz:4 blgp:2
	s_lshl_b32 s2, s37, 8
	v_lshl_add_u64 v[140:141], s[2:3], 2, v[190:191]
	s_lshl_b32 s2, s38, 11
	s_and_b32 s2, s2, 0x800
	s_waitcnt vmcnt(15)
	s_or_b32 s2, s2, 0x1e000
	s_add_i32 m0, s2, s22
	s_mul_i32 s18, s17, 0x5000
	global_load_lds_dword v[140:141], off
	s_waitcnt lgkmcnt(0)
	v_mfma_scale_f32_32x32x64_f8f6f4 v[112:127], v[146:149], v[172:177], v[112:127], v196, v194 op_sel_hi:[0,0,0] cbsz:4 blgp:2
	v_add_u32_e32 v144, s18, v212
	v_add_u32_e32 v145, s18, v209
	v_add_u32_e32 v150, s18, v208
	v_add_u32_e32 v213, s18, v211
	s_add_i32 s18, s17, 1
	s_cmp_lg_u32 s17, 5
	s_cselect_b32 s17, s18, 0
	v_mfma_scale_f32_32x32x64_f8f6f4 v[48:63], v[146:149], v[178:183], v[48:63], v196, v195 op_sel_hi:[0,0,0] cbsz:4 blgp:2
	ds_read_b128 v[140:143], v144
	ds_read_b128 v[146:149], v144 offset:1536
	ds_read_b64 v[144:145], v145
	ds_read_b64 v[150:151], v150
	v_mfma_scale_f32_32x32x64_f8f6f4 v[96:111], v[214:217], v[172:177], v[96:111], v197, v194 op_sel_hi:[0,0,0] cbsz:4 blgp:2
	v_mfma_scale_f32_32x32x64_f8f6f4 v[32:47], v[214:217], v[178:183], v[32:47], v197, v195 op_sel_hi:[0,0,0] cbsz:4 blgp:2
	v_mfma_scale_f32_32x32x64_f8f6f4 v[80:95], v[218:221], v[172:177], v[80:95], v192, v194 op_sel_hi:[0,0,0] cbsz:4 blgp:2
	v_mfma_scale_f32_32x32x64_f8f6f4 v[16:31], v[218:221], v[178:183], v[16:31], v192, v195 op_sel_hi:[0,0,0] cbsz:4 blgp:2
	v_mfma_scale_f32_32x32x64_f8f6f4 v[64:79], v[222:225], v[172:177], v[64:79], v193, v194 op_sel_hi:[0,0,0] cbsz:4 blgp:2
	ds_read_b128 v[168:171], v213
	ds_read_b128 v[172:175], v213 offset:1024
	ds_read_b128 v[214:217], v213 offset:2048
	ds_read_b128 v[218:221], v213 offset:3072
	v_mfma_scale_f32_32x32x64_f8f6f4 v[0:15], v[222:225], v[178:183], v[0:15], v193, v195 op_sel_hi:[0,0,0] cbsz:4 blgp:2
	s_waitcnt vmcnt(10)
	s_mul_i32 s18, s17, 0x5000
	s_waitcnt lgkmcnt(0)
	v_mfma_scale_f32_32x32x64_f8f6f4 v[112:127], v[168:171], v[140:145], v[112:127], v196, v194 op_sel_hi:[0,0,0] cbsz:4 blgp:2
	s_barrier
	v_add_u32_e32 v178, s18, v208
	v_add_u32_e32 v213, s18, v211
	v_mfma_scale_f32_32x32x64_f8f6f4 v[48:63], v[168:171], v[146:151], v[48:63], v196, v195 op_sel_hi:[0,0,0] cbsz:4 blgp:2
	v_mfma_scale_f32_32x32x64_f8f6f4 v[96:111], v[172:175], v[140:145], v[96:111], v197, v194 op_sel_hi:[0,0,0] cbsz:4 blgp:2
	v_mfma_scale_f32_32x32x64_f8f6f4 v[32:47], v[172:175], v[146:151], v[32:47], v197, v195 op_sel_hi:[0,0,0] cbsz:4 blgp:2
	v_add_u32_e32 v172, s18, v212
	v_add_u32_e32 v173, s18, v209
	ds_read_b128 v[168:171], v172
	ds_read_b128 v[174:177], v172 offset:1536
	ds_read_b64 v[172:173], v173
	ds_read_b64 v[178:179], v178
	s_add_i32 s18, s17, 1
	s_cmp_lg_u32 s17, 5
	s_cselect_b32 s17, s18, 0
	v_mfma_scale_f32_32x32x64_f8f6f4 v[80:95], v[214:217], v[140:145], v[80:95], v192, v194 op_sel_hi:[0,0,0] cbsz:4 blgp:2
	v_mfma_scale_f32_32x32x64_f8f6f4 v[16:31], v[214:217], v[146:151], v[16:31], v192, v195 op_sel_hi:[0,0,0] cbsz:4 blgp:2
	v_mfma_scale_f32_32x32x64_f8f6f4 v[64:79], v[218:221], v[140:145], v[64:79], v193, v194 op_sel_hi:[0,0,0] cbsz:4 blgp:2
	ds_read_b128 v[140:143], v213
	ds_read_b128 v[180:183], v213 offset:1024
	ds_read_b128 v[214:217], v213 offset:2048
	ds_read_b128 v[222:225], v213 offset:3072
	v_mfma_scale_f32_32x32x64_f8f6f4 v[0:15], v[218:221], v[146:151], v[0:15], v193, v195 op_sel_hi:[0,0,0] cbsz:4 blgp:2
	s_waitcnt vmcnt(15)
	s_mul_i32 s18, s17, 0x5000
	s_waitcnt lgkmcnt(0)
	v_mfma_scale_f32_32x32x64_f8f6f4 v[112:127], v[140:143], v[168:173], v[112:127], v196, v194 op_sel_hi:[0,0,0] cbsz:4 blgp:2
	v_add_u32_e32 v144, s18, v212
	v_add_u32_e32 v145, s18, v209
	v_add_u32_e32 v150, s18, v208
	v_add_u32_e32 v213, s18, v211
	v_mfma_scale_f32_32x32x64_f8f6f4 v[48:63], v[140:143], v[174:179], v[48:63], v196, v195 op_sel_hi:[0,0,0] cbsz:4 blgp:2
	ds_read_b128 v[140:143], v144
	ds_read_b128 v[146:149], v144 offset:1536
	ds_read_b64 v[144:145], v145
	ds_read_b64 v[150:151], v150
	s_add_i32 s18, s17, 1
	s_cmp_lg_u32 s17, 5
	s_cselect_b32 s39, s18, 0
	v_mfma_scale_f32_32x32x64_f8f6f4 v[96:111], v[180:183], v[168:173], v[96:111], v197, v194 op_sel_hi:[0,0,0] cbsz:4 blgp:2
	v_mfma_scale_f32_32x32x64_f8f6f4 v[32:47], v[180:183], v[174:179], v[32:47], v197, v195 op_sel_hi:[0,0,0] cbsz:4 blgp:2
	v_mfma_scale_f32_32x32x64_f8f6f4 v[80:95], v[214:217], v[168:173], v[80:95], v192, v194 op_sel_hi:[0,0,0] cbsz:4 blgp:2
	v_mfma_scale_f32_32x32x64_f8f6f4 v[16:31], v[214:217], v[174:179], v[16:31], v192, v195 op_sel_hi:[0,0,0] cbsz:4 blgp:2
	v_mfma_scale_f32_32x32x64_f8f6f4 v[64:79], v[222:225], v[168:173], v[64:79], v193, v194 op_sel_hi:[0,0,0] cbsz:4 blgp:2
	ds_read_b128 v[168:171], v213
	ds_read_b128 v[180:183], v213 offset:1024
	ds_read_b128 v[214:217], v213 offset:2048
	ds_read_b128 v[218:221], v213 offset:3072
	v_mfma_scale_f32_32x32x64_f8f6f4 v[0:15], v[222:225], v[174:179], v[0:15], v193, v195 op_sel_hi:[0,0,0] cbsz:4 blgp:2
	s_waitcnt vmcnt(0)
	s_mul_i32 s17, s39, 0x5000
	s_waitcnt lgkmcnt(0)
	v_mfma_scale_f32_32x32x64_f8f6f4 v[112:127], v[168:171], v[140:145], v[112:127], v196, v194 op_sel_hi:[0,0,0] cbsz:4 blgp:2
	s_barrier
	v_add_u32_e32 v172, s17, v212
	v_add_u32_e32 v173, s17, v209
	v_add_u32_e32 v178, s17, v208
	v_mfma_scale_f32_32x32x64_f8f6f4 v[48:63], v[168:171], v[146:151], v[48:63], v196, v195 op_sel_hi:[0,0,0] cbsz:4 blgp:2
	ds_read_b128 v[168:171], v172
	ds_read_b128 v[174:177], v172 offset:1536
	ds_read_b64 v[172:173], v173
	ds_read_b64 v[178:179], v178
	v_mfma_scale_f32_32x32x64_f8f6f4 v[96:111], v[180:183], v[140:145], v[96:111], v197, v194 op_sel_hi:[0,0,0] cbsz:4 blgp:2
	v_mfma_scale_f32_32x32x64_f8f6f4 v[32:47], v[180:183], v[146:151], v[32:47], v197, v195 op_sel_hi:[0,0,0] cbsz:4 blgp:2
	v_mfma_scale_f32_32x32x64_f8f6f4 v[80:95], v[214:217], v[140:145], v[80:95], v192, v194 op_sel_hi:[0,0,0] cbsz:4 blgp:2
	v_mfma_scale_f32_32x32x64_f8f6f4 v[16:31], v[214:217], v[146:151], v[16:31], v192, v195 op_sel_hi:[0,0,0] cbsz:4 blgp:2
	v_mfma_scale_f32_32x32x64_f8f6f4 v[64:79], v[218:221], v[140:145], v[64:79], v193, v194 op_sel_hi:[0,0,0] cbsz:4 blgp:2
	v_add_u32_e32 v144, s17, v211
	ds_read_b128 v[140:143], v144
	ds_read_b128 v[180:183], v144 offset:1024
	ds_read_b128 v[214:217], v144 offset:2048
	ds_read_b128 v[222:225], v144 offset:3072
	v_mfma_scale_f32_32x32x64_f8f6f4 v[0:15], v[218:221], v[146:151], v[0:15], v193, v195 op_sel_hi:[0,0,0] cbsz:4 blgp:2
	s_waitcnt lgkmcnt(0)
	v_mfma_scale_f32_32x32x64_f8f6f4 v[112:127], v[140:143], v[168:173], v[112:127], v196, v194 op_sel_hi:[0,0,0] cbsz:4 blgp:2
	s_waitcnt vmcnt(0)
	v_mfma_scale_f32_32x32x64_f8f6f4 v[48:63], v[140:143], v[174:179], v[48:63], v196, v195 op_sel_hi:[0,0,0] cbsz:4 blgp:2
	v_mfma_scale_f32_32x32x64_f8f6f4 v[96:111], v[180:183], v[168:173], v[96:111], v197, v194 op_sel_hi:[0,0,0] cbsz:4 blgp:2
	v_mfma_scale_f32_32x32x64_f8f6f4 v[32:47], v[180:183], v[174:179], v[32:47], v197, v195 op_sel_hi:[0,0,0] cbsz:4 blgp:2
	v_mfma_scale_f32_32x32x64_f8f6f4 v[80:95], v[214:217], v[168:173], v[80:95], v192, v194 op_sel_hi:[0,0,0] cbsz:4 blgp:2
	v_mfma_scale_f32_32x32x64_f8f6f4 v[16:31], v[214:217], v[174:179], v[16:31], v192, v195 op_sel_hi:[0,0,0] cbsz:4 blgp:2
	v_mfma_scale_f32_32x32x64_f8f6f4 v[64:79], v[222:225], v[168:173], v[64:79], v193, v194 op_sel_hi:[0,0,0] cbsz:4 blgp:2
	v_mfma_scale_f32_32x32x64_f8f6f4 v[0:15], v[222:225], v[174:179], v[0:15], v193, v195 op_sel_hi:[0,0,0] cbsz:4 blgp:2
	s_cmp_gt_u32 s74, 8
	s_cbranch_scc1 .Lge_skip_a
	s_waitcnt vmcnt(0)
	v_fmac_f32_e32 v244, v228, v236
	v_fmac_f32_e32 v244, v229, v237
	v_fmac_f32_e32 v244, v230, v238
	v_fmac_f32_e32 v244, v231, v239
	v_fmac_f32_e32 v244, v232, v240
	v_fmac_f32_e32 v244, v233, v241
	v_fmac_f32_e32 v244, v234, v242
	v_fmac_f32_e32 v244, v235, v243
	s_and_b32 s75, s74, 3
	s_cmp_lg_u32 s75, 0
	s_cbranch_scc1 .Lge_issue_a
	s_nop 1
	v_add_f32_dpp v244, v244, v244 quad_perm:[1,0,3,2] row_mask:0xf bank_mask:0xf
	s_nop 1
	v_add_f32_dpp v244, v244, v244 quad_perm:[2,3,0,1] row_mask:0xf bank_mask:0xf
	s_nop 1
	v_add_f32_dpp v244, v244, v244 row_half_mirror row_mask:0xf bank_mask:0xf
	s_nop 1
	v_add_f32_dpp v244, v244, v244 row_mirror row_mask:0xf bank_mask:0xf
	s_nop 1
	v_add_f32_dpp v244, v244, v244 row_bcast:15 row_mask:0xa bank_mask:0xf
	s_nop 1
	v_add_f32_dpp v244, v244, v244 row_bcast:31 row_mask:0xc bank_mask:0xf
	s_nop 1
	v_readlane_b32 s75, v244, 63
	v_mov_b32_e32 v247, 0
	s_mov_b64 s[80:81], exec
	s_nop 1
	v_mov_b32_e32 v246, s75
	s_mov_b64 exec, 1
	global_store_dword v247, v246, s[62:63]
	s_mov_b64 exec, s[80:81]
	s_add_u32 s62, s62, 4
	s_addc_u32 s63, s63, 0
	v_mov_b32_e32 v244, 0
	s_cmp_eq_u32 s74, 8
	s_cbranch_scc1 .Lge_done_a
	s_max_i32 s75, s77, 0
	s_min_i32 s75, s75, 0x7cff
	s_lshl_b32 s82, s75, 13
	s_add_u32 s84, s66, s82
	s_addc_u32 s85, s67, 0
	s_add_u32 s72, s72, 1
	s_lshl_b32 s82, s72, 13
	s_add_u32 s86, s64, s82
	s_addc_u32 s87, s65, 0
.Lge_issue_a:
	global_load_dwordx4 v[228:231], v245, s[84:85] nt
	global_load_dwordx4 v[232:235], v245, s[84:85] offset:1024 nt
	global_load_dwordx4 v[236:239], v245, s[86:87] nt
	global_load_dwordx4 v[240:243], v245, s[86:87] offset:1024 nt
	s_add_u32 s84, s84, 0x800
	s_addc_u32 s85, s85, 0
	s_add_u32 s86, s86, 0x800
	s_addc_u32 s87, s87, 0
.Lge_done_a:
	s_add_u32 s74, s74, 1
.Lge_skip_a:
	s_nop 3
	v_exp_f32_e32 v140, v112
	v_exp_f32_e32 v142, v113
	v_exp_f32_e32 v141, v48
	v_exp_f32_e32 v143, v49
	v_exp_f32_e32 v144, v114
	v_exp_f32_e32 v146, v115
	v_exp_f32_e32 v145, v50
	v_exp_f32_e32 v147, v51
	v_exp_f32_e32 v148, v116
	v_exp_f32_e32 v150, v117
	v_exp_f32_e32 v149, v52
	v_exp_f32_e32 v151, v53
	v_exp_f32_e32 v168, v118
	v_exp_f32_e32 v170, v119
	v_exp_f32_e32 v169, v54
	v_exp_f32_e32 v171, v55
	v_pk_add_f32 v[140:141], v[140:141], 0 op_sel_hi:[1,0]
	v_pk_add_f32 v[142:143], v[142:143], 0 op_sel_hi:[1,0]
	v_exp_f32_e32 v172, v120
	v_exp_f32_e32 v174, v121
	v_exp_f32_e32 v173, v56
	v_exp_f32_e32 v175, v57
	v_exp_f32_e32 v176, v122
	v_exp_f32_e32 v178, v123
	v_exp_f32_e32 v177, v58
	v_exp_f32_e32 v179, v59
	v_pk_add_f32 v[140:141], v[144:145], v[140:141]
	v_pk_add_f32 v[142:143], v[146:147], v[142:143]
	v_exp_f32_e32 v180, v124
	v_exp_f32_e32 v182, v125
	v_exp_f32_e32 v181, v60
	v_exp_f32_e32 v183, v61
	v_pk_add_f32 v[140:141], v[148:149], v[140:141]
	v_pk_add_f32 v[142:143], v[150:151], v[142:143]
	v_exp_f32_e32 v192, v126
	v_exp_f32_e32 v194, v127
	v_exp_f32_e32 v193, v62
	v_exp_f32_e32 v195, v63
	v_pk_add_f32 v[140:141], v[168:169], v[140:141]
	v_pk_add_f32 v[142:143], v[170:171], v[142:143]
	v_exp_f32_e32 v196, v96
	v_exp_f32_e32 v214, v97
	v_exp_f32_e32 v197, v32
	v_exp_f32_e32 v215, v33
	v_pk_add_f32 v[140:141], v[172:173], v[140:141]
	v_pk_add_f32 v[142:143], v[174:175], v[142:143]
	v_exp_f32_e32 v216, v98
	v_exp_f32_e32 v218, v99
	v_exp_f32_e32 v217, v34
	v_exp_f32_e32 v219, v35
	v_pk_add_f32 v[140:141], v[176:177], v[140:141]
	v_pk_add_f32 v[142:143], v[178:179], v[142:143]
	v_exp_f32_e32 v220, v100
	v_exp_f32_e32 v222, v101
	v_exp_f32_e32 v221, v36
	v_exp_f32_e32 v223, v37
	v_pk_add_f32 v[140:141], v[180:181], v[140:141]
	v_pk_add_f32 v[142:143], v[182:183], v[142:143]
	v_exp_f32_e32 v224, v102
	v_exp_f32_e32 v226, v103
	v_exp_f32_e32 v225, v38
	v_pk_add_f32 v[140:141], v[192:193], v[140:141]
	v_exp_f32_e32 v227, v39
	v_pk_add_f32 v[142:143], v[194:195], v[142:143]
	v_pk_add_f32 v[140:141], v[196:197], v[140:141]
	v_pk_add_f32 v[142:143], v[214:215], v[142:143]
	v_exp_f32_e32 v144, v104
	v_exp_f32_e32 v146, v105
	v_exp_f32_e32 v145, v40
	v_exp_f32_e32 v147, v41
	v_pk_add_f32 v[140:141], v[216:217], v[140:141]
	v_pk_add_f32 v[142:143], v[218:219], v[142:143]
	v_exp_f32_e32 v148, v106
	v_exp_f32_e32 v150, v107
	v_exp_f32_e32 v149, v42
	v_exp_f32_e32 v151, v43
	v_pk_add_f32 v[140:141], v[220:221], v[140:141]
	v_pk_add_f32 v[142:143], v[222:223], v[142:143]
	v_exp_f32_e32 v168, v108
	v_exp_f32_e32 v170, v109
	v_exp_f32_e32 v169, v44
	v_exp_f32_e32 v171, v45
	v_pk_add_f32 v[140:141], v[224:225], v[140:141]
	v_pk_add_f32 v[142:143], v[226:227], v[142:143]
	v_exp_f32_e32 v172, v110
	v_exp_f32_e32 v174, v111
	v_exp_f32_e32 v173, v46
	v_exp_f32_e32 v175, v47
	v_exp_f32_e32 v176, v80
	v_exp_f32_e32 v178, v81
	v_exp_f32_e32 v177, v16
	v_exp_f32_e32 v179, v17
	v_pk_add_f32 v[140:141], v[144:145], v[140:141]
	v_pk_add_f32 v[142:143], v[146:147], v[142:143]
	v_exp_f32_e32 v180, v82
	v_exp_f32_e32 v182, v83
	v_exp_f32_e32 v181, v18
	v_exp_f32_e32 v183, v19
	v_pk_add_f32 v[140:141], v[148:149], v[140:141]
	v_pk_add_f32 v[142:143], v[150:151], v[142:143]
	v_exp_f32_e32 v192, v84
	v_exp_f32_e32 v194, v85
	v_exp_f32_e32 v193, v20
	v_exp_f32_e32 v195, v21
	v_pk_add_f32 v[140:141], v[168:169], v[140:141]
	v_pk_add_f32 v[142:143], v[170:171], v[142:143]
	v_exp_f32_e32 v196, v86
	v_exp_f32_e32 v214, v87
	v_exp_f32_e32 v197, v22
	v_exp_f32_e32 v215, v23
	v_pk_add_f32 v[140:141], v[172:173], v[140:141]
	v_pk_add_f32 v[142:143], v[174:175], v[142:143]
	v_exp_f32_e32 v216, v88
	v_exp_f32_e32 v218, v89
	v_exp_f32_e32 v217, v24
	v_exp_f32_e32 v219, v25
	v_pk_add_f32 v[140:141], v[176:177], v[140:141]
	v_pk_add_f32 v[142:143], v[178:179], v[142:143]
	v_exp_f32_e32 v220, v90
	v_exp_f32_e32 v222, v91
	v_exp_f32_e32 v221, v26
	v_exp_f32_e32 v223, v27
	v_pk_add_f32 v[140:141], v[180:181], v[140:141]
	v_pk_add_f32 v[142:143], v[182:183], v[142:143]
	v_exp_f32_e32 v224, v92
	v_exp_f32_e32 v226, v93
	v_exp_f32_e32 v225, v28
	v_pk_add_f32 v[140:141], v[192:193], v[140:141]
	v_exp_f32_e32 v227, v29
	v_pk_add_f32 v[142:143], v[194:195], v[142:143]
	v_pk_add_f32 v[140:141], v[196:197], v[140:141]
	v_pk_add_f32 v[142:143], v[214:215], v[142:143]
	v_exp_f32_e32 v146, v94
	v_exp_f32_e32 v148, v95
	v_exp_f32_e32 v147, v30
	v_exp_f32_e32 v149, v31
	v_pk_add_f32 v[140:141], v[216:217], v[140:141]
	v_pk_add_f32 v[142:143], v[218:219], v[142:143]
	v_exp_f32_e32 v150, v64
	v_exp_f32_e32 v168, v65
	v_exp_f32_e32 v151, v0
	v_exp_f32_e32 v169, v1
	v_pk_add_f32 v[140:141], v[220:221], v[140:141]
	v_pk_add_f32 v[142:143], v[222:223], v[142:143]
	v_exp_f32_e32 v170, v66
	v_exp_f32_e32 v172, v67
	v_exp_f32_e32 v171, v2
	v_exp_f32_e32 v173, v3
	v_pk_add_f32 v[140:141], v[224:225], v[140:141]
	v_pk_add_f32 v[142:143], v[226:227], v[142:143]
	v_exp_f32_e32 v174, v68
	v_exp_f32_e32 v176, v69
	v_exp_f32_e32 v175, v4
	v_exp_f32_e32 v177, v5
	v_exp_f32_e32 v178, v70
	v_exp_f32_e32 v180, v71
	v_exp_f32_e32 v179, v6
	v_exp_f32_e32 v181, v7
	v_pk_add_f32 v[140:141], v[146:147], v[140:141]
	v_pk_add_f32 v[142:143], v[148:149], v[142:143]
	v_exp_f32_e32 v182, v72
	v_exp_f32_e32 v192, v73
	v_exp_f32_e32 v183, v8
	v_exp_f32_e32 v193, v9
	v_pk_add_f32 v[140:141], v[150:151], v[140:141]
	v_pk_add_f32 v[142:143], v[168:169], v[142:143]
	v_exp_f32_e32 v194, v74
	v_exp_f32_e32 v196, v75
	v_exp_f32_e32 v195, v10
	v_exp_f32_e32 v197, v11
	v_pk_add_f32 v[140:141], v[170:171], v[140:141]
	v_pk_add_f32 v[142:143], v[172:173], v[142:143]
	v_exp_f32_e32 v214, v76
	v_exp_f32_e32 v216, v77
	v_exp_f32_e32 v215, v12
	v_exp_f32_e32 v217, v13
	v_pk_add_f32 v[140:141], v[174:175], v[140:141]
	v_pk_add_f32 v[142:143], v[176:177], v[142:143]
	v_exp_f32_e32 v218, v78
	v_exp_f32_e32 v220, v79
	v_exp_f32_e32 v219, v14
	v_exp_f32_e32 v221, v15
	v_pk_add_f32 v[140:141], v[178:179], v[140:141]
	v_pk_add_f32 v[142:143], v[180:181], v[142:143]
	v_and_b32_e32 v145, 64, v187
	v_pk_add_f32 v[140:141], v[182:183], v[140:141]
	v_pk_add_f32 v[142:143], v[192:193], v[142:143]
	v_xor_b32_e32 v144, 32, v187
	v_add_u32_e32 v145, 64, v145
	v_pk_add_f32 v[140:141], v[194:195], v[140:141]
	v_pk_add_f32 v[142:143], v[196:197], v[142:143]
	v_cmp_lt_i32_e32 vcc, v144, v145
	v_pk_add_f32 v[140:141], v[214:215], v[140:141]
	v_pk_add_f32 v[142:143], v[216:217], v[142:143]
	v_cndmask_b32_e32 v144, v187, v144, vcc
	v_pk_add_f32 v[140:141], v[218:219], v[140:141]
	v_pk_add_f32 v[142:143], v[220:221], v[142:143]
	v_lshlrev_b32_e32 v144, 2, v144
	v_pk_add_f32 v[140:141], v[140:141], v[142:143]
	ds_bpermute_b32 v142, v144, v140
	ds_bpermute_b32 v143, v144, v141
	s_lshl_b32 s16, s16, 8
	s_or_b32 s16, s16, s33
	s_waitcnt lgkmcnt(0)
	v_pk_add_f32 v[140:141], v[140:141], v[142:143]
	s_nop 0
	v_cmp_nge_f32_e32 vcc, s34, v141
	s_nop 1
	v_cndmask_b32_e64 v142, 0, 1, vcc
	v_cmp_nge_f32_e32 vcc, s34, v140
	v_lshlrev_b16_e32 v142, 1, v142
	s_nop 0
	v_cndmask_b32_e64 v143, 0, 1, vcc
	v_cmp_nle_f32_e32 vcc, s35, v140
	v_bitop3_b16 v142, v143, 3, v142 bitop3:0xc8
	s_nop 0
	v_cndmask_b32_e64 v143, 0, 1, vcc
	v_cmp_nle_f32_e32 vcc, s35, v141
	v_lshlrev_b16_e32 v143, 2, v143
	s_nop 0
	v_cndmask_b32_e64 v145, 0, 1, vcc
	v_lshlrev_b16_e32 v145, 3, v145
	v_or_b32_e32 v143, v145, v143
	v_bitop3_b16 v142, v142, 15, v143 bitop3:0xc8
	v_cmp_ne_u16_e32 vcc, 0, v142
	s_cbranch_vccz .LBB1_23
	v_max_f32_e32 v142, v113, v113
	v_max_f32_e32 v143, v112, v112
	v_max_f32_e32 v142, v143, v142
	v_max3_f32 v142, v142, v114, v115
	v_max3_f32 v142, v142, v116, v117
	v_max3_f32 v142, v142, v118, v119
	v_max3_f32 v142, v142, v120, v121
	v_max3_f32 v142, v142, v122, v123
	v_max3_f32 v142, v142, v124, v125
	v_max3_f32 v142, v142, v126, v127
	v_max3_f32 v142, v142, v96, v97
	v_max3_f32 v142, v142, v98, v99
	v_max3_f32 v142, v142, v100, v101
	v_max3_f32 v142, v142, v102, v103
	v_max3_f32 v142, v142, v104, v105
	v_max3_f32 v142, v142, v106, v107
	v_max3_f32 v142, v142, v108, v109
	v_max3_f32 v142, v142, v110, v111
	v_max3_f32 v142, v142, v80, v81
	v_max3_f32 v142, v142, v82, v83
	v_max3_f32 v142, v142, v84, v85
	v_max3_f32 v142, v142, v86, v87
	v_max3_f32 v142, v142, v88, v89
	v_max3_f32 v142, v142, v90, v91
	v_max3_f32 v142, v142, v92, v93
	v_max3_f32 v142, v142, v94, v95
	v_max3_f32 v142, v142, v64, v65
	v_max3_f32 v142, v142, v66, v67
	v_max3_f32 v142, v142, v68, v69
	v_max3_f32 v142, v142, v70, v71
	v_max3_f32 v142, v142, v72, v73
	v_max3_f32 v142, v142, v74, v75
	v_max3_f32 v142, v142, v76, v77
	v_max3_f32 v142, v142, v78, v79
	ds_bpermute_b32 v143, v144, v142
	s_waitcnt lgkmcnt(0)
	v_max_f32_e32 v143, v143, v143
	v_max_f32_e32 v142, v142, v143
	v_sub_f32_e32 v112, v112, v142
	v_sub_f32_e32 v113, v113, v142
	v_exp_f32_e32 v112, v112
	v_sub_f32_e32 v114, v114, v142
	v_exp_f32_e32 v113, v113
	v_sub_f32_e32 v115, v115, v142
	v_exp_f32_e32 v114, v114
	v_exp_f32_e32 v115, v115
	v_add_f32_e32 v112, 0, v112
	v_add_f32_e32 v112, v113, v112
	v_sub_f32_e32 v113, v116, v142
	v_add_f32_e32 v112, v114, v112
	v_exp_f32_e32 v113, v113
	v_sub_f32_e32 v114, v117, v142
	v_add_f32_e32 v112, v115, v112
	v_exp_f32_e32 v114, v114
	v_sub_f32_e32 v115, v118, v142
	v_exp_f32_e32 v115, v115
	v_sub_f32_e32 v116, v119, v142
	v_exp_f32_e32 v116, v116
	v_add_f32_e32 v112, v113, v112
	v_sub_f32_e32 v113, v120, v142
	v_add_f32_e32 v112, v114, v112
	v_exp_f32_e32 v113, v113
	v_sub_f32_e32 v114, v121, v142
	v_add_f32_e32 v112, v115, v112
	v_exp_f32_e32 v114, v114
	v_sub_f32_e32 v115, v122, v142
	v_add_f32_e32 v112, v116, v112
	v_exp_f32_e32 v115, v115
	v_sub_f32_e32 v116, v123, v142
	v_exp_f32_e32 v116, v116
	v_add_f32_e32 v112, v113, v112
	v_sub_f32_e32 v113, v124, v142
	v_add_f32_e32 v112, v114, v112
	v_exp_f32_e32 v113, v113
	v_sub_f32_e32 v114, v125, v142
	v_add_f32_e32 v112, v115, v112
	v_exp_f32_e32 v114, v114
	v_sub_f32_e32 v115, v126, v142
	v_add_f32_e32 v112, v116, v112
	v_exp_f32_e32 v115, v115
	v_sub_f32_e32 v116, v127, v142
	v_exp_f32_e32 v116, v116
	v_sub_f32_e32 v96, v96, v142
	v_add_f32_e32 v112, v113, v112
	v_exp_f32_e32 v96, v96
	v_sub_f32_e32 v97, v97, v142
	v_add_f32_e32 v112, v114, v112
	v_exp_f32_e32 v97, v97
	v_sub_f32_e32 v98, v98, v142
	v_add_f32_e32 v112, v115, v112
	v_exp_f32_e32 v98, v98
	v_sub_f32_e32 v99, v99, v142
	v_add_f32_e32 v112, v116, v112
	v_exp_f32_e32 v99, v99
	v_add_f32_e32 v96, v96, v112
	v_add_f32_e32 v96, v97, v96
	v_sub_f32_e32 v97, v100, v142
	v_add_f32_e32 v96, v98, v96
	v_exp_f32_e32 v97, v97
	v_sub_f32_e32 v98, v101, v142
	v_add_f32_e32 v96, v99, v96
	v_exp_f32_e32 v98, v98
	v_sub_f32_e32 v99, v102, v142
	v_exp_f32_e32 v99, v99
	v_sub_f32_e32 v100, v103, v142
	v_exp_f32_e32 v100, v100
	v_add_f32_e32 v96, v97, v96
	v_sub_f32_e32 v97, v104, v142
	v_add_f32_e32 v96, v98, v96
	v_exp_f32_e32 v97, v97
	v_sub_f32_e32 v98, v105, v142
	v_add_f32_e32 v96, v99, v96
	v_exp_f32_e32 v98, v98
	v_sub_f32_e32 v99, v106, v142
	v_add_f32_e32 v96, v100, v96
	v_exp_f32_e32 v99, v99
	v_sub_f32_e32 v100, v107, v142
	v_exp_f32_e32 v100, v100
	v_add_f32_e32 v96, v97, v96
	v_sub_f32_e32 v97, v108, v142
	v_add_f32_e32 v96, v98, v96
	v_exp_f32_e32 v97, v97
	v_sub_f32_e32 v98, v109, v142
	v_add_f32_e32 v96, v99, v96
	v_exp_f32_e32 v98, v98
	v_sub_f32_e32 v99, v110, v142
	v_add_f32_e32 v96, v100, v96
	v_exp_f32_e32 v99, v99
	v_sub_f32_e32 v100, v111, v142
	v_exp_f32_e32 v100, v100
	v_sub_f32_e32 v80, v80, v142
	v_add_f32_e32 v96, v97, v96
	v_exp_f32_e32 v80, v80
	v_sub_f32_e32 v81, v81, v142
	v_add_f32_e32 v96, v98, v96
	v_exp_f32_e32 v81, v81
	v_sub_f32_e32 v82, v82, v142
	v_add_f32_e32 v96, v99, v96
	v_exp_f32_e32 v82, v82
	v_sub_f32_e32 v83, v83, v142
	v_add_f32_e32 v96, v100, v96
	v_exp_f32_e32 v83, v83
	v_add_f32_e32 v80, v80, v96
	v_add_f32_e32 v80, v81, v80
	v_sub_f32_e32 v81, v84, v142
	v_add_f32_e32 v80, v82, v80
	v_exp_f32_e32 v81, v81
	v_sub_f32_e32 v82, v85, v142
	v_add_f32_e32 v80, v83, v80
	v_exp_f32_e32 v82, v82
	v_sub_f32_e32 v83, v86, v142
	v_exp_f32_e32 v83, v83
	v_sub_f32_e32 v84, v87, v142
	v_exp_f32_e32 v84, v84
	v_add_f32_e32 v80, v81, v80
	v_sub_f32_e32 v81, v88, v142
	v_add_f32_e32 v80, v82, v80
	v_exp_f32_e32 v81, v81
	v_sub_f32_e32 v82, v89, v142
	v_add_f32_e32 v80, v83, v80
	v_exp_f32_e32 v82, v82
	v_sub_f32_e32 v83, v90, v142
	v_add_f32_e32 v80, v84, v80
	v_exp_f32_e32 v83, v83
	v_sub_f32_e32 v84, v91, v142
	v_exp_f32_e32 v84, v84
	v_add_f32_e32 v80, v81, v80
	v_sub_f32_e32 v81, v92, v142
	v_add_f32_e32 v80, v82, v80
	v_exp_f32_e32 v81, v81
	v_sub_f32_e32 v82, v93, v142
	v_add_f32_e32 v80, v83, v80
	v_exp_f32_e32 v82, v82
	v_sub_f32_e32 v83, v94, v142
	v_add_f32_e32 v80, v84, v80
	v_exp_f32_e32 v83, v83
	v_sub_f32_e32 v84, v95, v142
	v_exp_f32_e32 v84, v84
	v_sub_f32_e32 v64, v64, v142
	v_add_f32_e32 v80, v81, v80
	v_exp_f32_e32 v64, v64
	v_sub_f32_e32 v65, v65, v142
	v_add_f32_e32 v80, v82, v80
	v_exp_f32_e32 v65, v65
	v_sub_f32_e32 v66, v66, v142
	v_add_f32_e32 v80, v83, v80
	v_exp_f32_e32 v66, v66
	v_sub_f32_e32 v67, v67, v142
	v_add_f32_e32 v80, v84, v80
	v_exp_f32_e32 v67, v67
	v_add_f32_e32 v64, v64, v80
	v_add_f32_e32 v64, v65, v64
	v_sub_f32_e32 v65, v68, v142
	v_add_f32_e32 v64, v66, v64
	v_exp_f32_e32 v65, v65
	v_sub_f32_e32 v66, v69, v142
	v_add_f32_e32 v64, v67, v64
	v_exp_f32_e32 v66, v66
	v_sub_f32_e32 v67, v70, v142
	v_exp_f32_e32 v67, v67
	v_sub_f32_e32 v68, v71, v142
	v_exp_f32_e32 v68, v68
	v_add_f32_e32 v64, v65, v64
	v_sub_f32_e32 v65, v72, v142
	v_add_f32_e32 v64, v66, v64
	v_exp_f32_e32 v65, v65
	v_sub_f32_e32 v66, v73, v142
	v_add_f32_e32 v64, v67, v64
	v_exp_f32_e32 v66, v66
	v_sub_f32_e32 v67, v74, v142
	v_add_f32_e32 v64, v68, v64
	v_exp_f32_e32 v67, v67
	v_sub_f32_e32 v68, v75, v142
	v_exp_f32_e32 v68, v68
	v_add_f32_e32 v64, v65, v64
	v_sub_f32_e32 v65, v76, v142
	v_add_f32_e32 v64, v66, v64
	v_exp_f32_e32 v65, v65
	v_sub_f32_e32 v66, v77, v142
	v_add_f32_e32 v64, v67, v64
	v_exp_f32_e32 v66, v66
	v_sub_f32_e32 v67, v78, v142
	v_add_f32_e32 v64, v68, v64
	v_exp_f32_e32 v67, v67
	v_sub_f32_e32 v68, v79, v142
	v_exp_f32_e32 v68, v68
	v_add_f32_e32 v64, v65, v64
	v_add_f32_e32 v64, v66, v64
	v_add_f32_e32 v64, v67, v64
	v_add_f32_e32 v64, v68, v64
	ds_bpermute_b32 v65, v144, v64
	s_and_saveexec_b64 s[18:19], s[0:1]
	s_cbranch_execz .LBB1_20
	v_or_b32_e32 v66, s16, v184
	v_ashrrev_i32_e32 v67, 31, v66
	v_lshl_add_u64 v[68:69], v[66:67], 2, s[8:9]
	global_atomic_add v68, v[68:69], v207, off sc0
	s_waitcnt lgkmcnt(0)
	v_add_f32_e32 v143, v64, v65
	v_mov_b64_e32 v[64:65], s[10:11]
	v_mad_i64_i32 v[64:65], s[40:41], v66, s36, v[64:65]
	s_waitcnt vmcnt(0)
	v_ashrrev_i32_e32 v69, 31, v68
	v_lshl_add_u64 v[64:65], v[68:69], 3, v[64:65]
	global_store_dwordx2 v[64:65], v[142:143], off

.LBB1_26:
	s_and_b64 vcc, exec, s[18:19]
	s_cbranch_vccz .LBB1_43
	s_waitcnt lgkmcnt(0)
	s_load_dwordx4 s[64:67], s[60:61], 0x40
	s_load_dwordx2 s[68:69], s[60:61], 0x50
	s_lshl_b32 s72, s59, 4
	s_lshr_b32 s73, s58, 6
	s_lshl_b32 s73, s73, 1
	s_add_u32 s72, s72, s73
	s_lshl_b32 s73, s72, 2
	s_sub_u32 s62, s62, 0x4000
	s_subb_u32 s63, s63, 0
	s_add_u32 s62, s62, s73
	s_addc_u32 s63, s63, 0
	s_waitcnt lgkmcnt(0)
	s_add_u32 s68, s68, s73
	s_addc_u32 s69, s69, 0
	s_load_dwordx2 s[76:77], s[68:69], 0x0
	v_mbcnt_lo_u32_b32 v245, -1, 0
	v_mbcnt_hi_u32_b32 v245, -1, v245
	v_lshlrev_b32_e32 v245, 4, v245
	v_mov_b32_e32 v244, 0
	s_waitcnt lgkmcnt(0)
	s_max_i32 s75, s76, 0
	s_min_i32 s75, s75, 0x7cff
	s_lshl_b32 s82, s75, 13
	s_add_u32 s84, s66, s82
	s_addc_u32 s85, s67, 0
	s_lshl_b32 s82, s72, 13
	s_add_u32 s86, s64, s82
	s_addc_u32 s87, s65, 0
	global_load_dwordx4 v[228:231], v245, s[84:85] nt
	global_load_dwordx4 v[232:235], v245, s[84:85] offset:1024 nt
	global_load_dwordx4 v[236:239], v245, s[86:87] nt
	global_load_dwordx4 v[240:243], v245, s[86:87] offset:1024 nt
	s_add_u32 s84, s84, 0x800
	s_addc_u32 s85, s85, 0
	s_add_u32 s86, s86, 0x800
	s_addc_u32 s87, s87, 0
	s_mov_b32 s74, 1
	v_lshlrev_b32_e32 v178, 2, v205
	s_waitcnt lgkmcnt(0)
	v_add_u32_e32 v0, s29, v178
	v_add_u32_e32 v0, 0x400, v0
	v_or_b32_e32 v1, 0x1e180, v178
	ds_read2_b32 v[172:173], v0 offset1:32
	v_or_b32_e32 v0, 0x1e000, v178
	v_or_b32_e32 v2, 0x1e100, v178
	v_or_b32_e32 v3, 0x1e080, v178
	ds_read_b32 v175, v1
	ds_read_b32 v174, v2
	ds_read_b32 v177, v3
	ds_read_b32 v176, v0
	v_mov_b32_e32 v187, 0
	v_lshl_add_u64 v[168:169], s[14:15], 0, v[186:187]
	s_and_b32 s15, s28, 0xc0
	s_or_b32 s16, s21, 0x1f40000
	s_bfe_u32 s14, s20, 0x20003
	s_lshl_b32 s0, s15, 2
	s_add_u32 s0, s12, s0
	s_addc_u32 s1, s13, 0
	s_mov_b32 s3, 0
	v_lshl_add_u64 v[170:171], s[0:1], 0, v[186:187]
	v_cmp_gt_u32_e64 s[0:1], 32, v184
	s_mov_b32 s33, 5
	s_mov_b32 s30, 1
	v_mbcnt_hi_u32_b32 v179, -1, v204
	s_mov_b32 s17, 0x71800000
	s_mov_b32 s18, 0xd800000
	v_mov_b32_e32 v180, 1
	s_movk_i32 s19, 0x7d0
	s_mov_b32 s28, 0
	s_branch .LBB1_29

.LBB1_33:
	s_mul_i32 s12, s33, 0x5000
	s_waitcnt vmcnt(10)
	s_add_i32 s12, s21, s12
	s_waitcnt lgkmcnt(0)
	s_barrier
	s_add_i32 s13, s27, 0xa000
	s_mov_b32 m0, s12
	s_waitcnt lgkmcnt(0)
	v_mfma_scale_f32_32x32x64_f8f6f4 v[80:95], v[156:159], v[134:139], 0, v174, v172 op_sel_hi:[0,0,0] cbsz:4 blgp:2
	buffer_load_dwordx4 v200, s[4:7], s13 offen lds
	s_add_i32 m0, s12, 0x1000
	s_add_i32 s13, s27, 0xb000
	buffer_load_dwordx4 v200, s[4:7], s13 offen lds
	s_add_i32 m0, s12, 0x2000
	s_add_i32 s13, s23, 0xf000
	buffer_load_dwordx4 v200, s[4:7], s13 offen lds
	s_add_i32 m0, s12, 0x3000
	s_add_i32 s13, s23, 0x10000
	buffer_load_dwordx4 v200, s[4:7], s13 offen lds
	s_add_i32 m0, s12, 0x4000
	s_add_i32 s12, s23, 0x11000
	buffer_load_dwordx4 v200, s[4:7], s12 offen lds
	s_mul_i32 s12, s30, 0x5000
	v_add_u32_e32 v0, s12, v202
	v_add_u32_e32 v1, s12, v198
	v_mfma_scale_f32_32x32x64_f8f6f4 v[16:31], v[156:159], v[128:133], 0, v174, v173 op_sel_hi:[0,0,0] cbsz:4 blgp:2
	ds_read_b128 v[140:143], v0
	ds_read_b128 v[156:159], v0 offset:1536
	v_add_u32_e32 v0, s12, v199
	s_add_i32 s13, s33, 1
	s_cmp_lg_u32 s33, 5
	s_cselect_b32 s13, s13, 0
	s_add_i32 s31, s30, 1
	s_cmp_lg_u32 s30, 5
	v_mfma_scale_f32_32x32x64_f8f6f4 v[96:111], v[160:163], v[134:139], 0, v177, v172 op_sel_hi:[0,0,0] cbsz:4 blgp:2
	s_cselect_b32 s31, s31, 0
	v_mfma_scale_f32_32x32x64_f8f6f4 v[32:47], v[160:163], v[128:133], 0, v177, v173 op_sel_hi:[0,0,0] cbsz:4 blgp:2
	ds_read_b64 v[144:145], v1
	ds_read_b64 v[160:161], v0
	v_add_u32_e32 v0, s12, v201
	s_mov_b32 s12, 0
	v_mfma_scale_f32_32x32x64_f8f6f4 v[112:127], v[164:167], v[134:139], 0, v176, v172 op_sel_hi:[0,0,0] cbsz:4 blgp:2
	v_mfma_scale_f32_32x32x64_f8f6f4 v[48:63], v[164:167], v[128:133], 0, v176, v173 op_sel_hi:[0,0,0] cbsz:4 blgp:2
	ds_read_b128 v[146:149], v0
	ds_read_b128 v[162:165], v0 offset:1024
	v_mfma_scale_f32_32x32x64_f8f6f4 v[64:79], v[152:155], v[134:139], 0, v175, v172 op_sel_hi:[0,0,0] cbsz:4 blgp:2
	ds_read_b128 v[134:137], v0 offset:2048
	ds_read_b128 v[188:191], v0 offset:3072
	v_mfma_scale_f32_32x32x64_f8f6f4 v[0:15], v[152:155], v[128:133], 0, v175, v173 op_sel_hi:[0,0,0] cbsz:4 blgp:2
	s_mul_i32 s30, s13, 0x5000
	s_waitcnt vmcnt(15)
	s_add_i32 s30, s21, s30
	s_add_i32 s33, s27, 0xc000
	s_mov_b32 m0, s30
	s_waitcnt lgkmcnt(0)
	v_mfma_scale_f32_32x32x64_f8f6f4 v[112:127], v[146:149], v[140:145], v[112:127], v176, v172 op_sel_hi:[0,0,0] cbsz:4 blgp:2
	buffer_load_dwordx4 v200, s[4:7], s33 offen lds
	s_add_i32 m0, s30, 0x1000
	s_add_i32 s33, s27, 0xd000
	buffer_load_dwordx4 v200, s[4:7], s33 offen lds
	s_add_i32 m0, s30, 0x2000
	s_add_i32 s33, s23, 0x12000
	buffer_load_dwordx4 v200, s[4:7], s33 offen lds
	s_add_i32 m0, s30, 0x3000
	s_add_i32 s33, s23, 0x13000
	buffer_load_dwordx4 v200, s[4:7], s33 offen lds
	s_add_i32 m0, s30, 0x4000
	s_add_i32 s30, s23, 0x14000
	buffer_load_dwordx4 v200, s[4:7], s30 offen lds
	v_mfma_scale_f32_32x32x64_f8f6f4 v[48:63], v[146:149], v[156:161], v[48:63], v176, v173 op_sel_hi:[0,0,0] cbsz:4 blgp:2
	s_mul_i32 s33, s31, 0x5000
	v_add_u32_e32 v128, s33, v202
	v_add_u32_e32 v132, s33, v198
	v_add_u32_e32 v133, s33, v199
	s_add_i32 s30, s13, 1
	s_cmp_lg_u32 s13, 5
	s_cselect_b32 s30, s30, 0
	v_mfma_scale_f32_32x32x64_f8f6f4 v[96:111], v[162:165], v[140:145], v[96:111], v177, v172 op_sel_hi:[0,0,0] cbsz:4 blgp:2
	s_add_i32 s13, s31, 1
	s_cmp_lg_u32 s31, 5
	s_cselect_b32 s13, s13, 0
	v_mfma_scale_f32_32x32x64_f8f6f4 v[32:47], v[162:165], v[156:161], v[32:47], v177, v173 op_sel_hi:[0,0,0] cbsz:4 blgp:2
	v_add_u32_e32 v162, s33, v201
	v_mfma_scale_f32_32x32x64_f8f6f4 v[80:95], v[134:137], v[140:145], v[80:95], v174, v172 op_sel_hi:[0,0,0] cbsz:4 blgp:2
	v_mfma_scale_f32_32x32x64_f8f6f4 v[16:31], v[134:137], v[156:161], v[16:31], v174, v173 op_sel_hi:[0,0,0] cbsz:4 blgp:2
	ds_read_b128 v[134:137], v128
	ds_read_b128 v[128:131], v128 offset:1536
	ds_read_b64 v[138:139], v132
	ds_read_b64 v[132:133], v133
	ds_read_b128 v[152:155], v162
	ds_read_b128 v[148:151], v162 offset:1024
	v_mfma_scale_f32_32x32x64_f8f6f4 v[64:79], v[188:191], v[140:145], v[64:79], v175, v172 op_sel_hi:[0,0,0] cbsz:4 blgp:2
	ds_read_b128 v[144:147], v162 offset:2048
	ds_read_b128 v[140:143], v162 offset:3072
	v_mfma_scale_f32_32x32x64_f8f6f4 v[0:15], v[188:191], v[156:161], v[0:15], v175, v173 op_sel_hi:[0,0,0] cbsz:4 blgp:2
	s_add_i32 s31, s27, 0x11000
	s_add_i32 s33, s23, 0x1a000
.LBB1_34:
	s_mul_i32 s34, s30, 0x5000
	s_waitcnt vmcnt(10)
	s_add_i32 s43, s21, s34
	s_waitcnt lgkmcnt(0)
	s_barrier
	s_add_i32 s42, s31, 0xffffd000
	s_mov_b32 m0, s43
	s_waitcnt lgkmcnt(0)
	v_mfma_scale_f32_32x32x64_f8f6f4 v[112:127], v[152:155], v[134:139], v[112:127], v176, v172 op_sel_hi:[0,0,0] cbsz:4 blgp:2
	buffer_load_dwordx4 v200, s[4:7], s42 offen lds
	s_add_i32 m0, s43, 0x1000
	s_add_i32 s42, s31, 0xffffe000
	v_mfma_scale_f32_32x32x64_f8f6f4 v[48:63], v[152:155], v[128:133], v[48:63], v176, v173 op_sel_hi:[0,0,0] cbsz:4 blgp:2
	buffer_load_dwordx4 v200, s[4:7], s42 offen lds
	s_add_i32 m0, s43, 0x2000
	s_add_i32 s42, s33, 0xffffb000
	s_mul_i32 s35, s13, 0x5000
	v_add_u32_e32 v152, s35, v201
	s_add_i32 s34, s30, 1
	s_cmp_lg_u32 s30, 5
	s_cselect_b32 s30, s34, 0
	s_add_i32 s34, s13, 1
	s_cmp_lg_u32 s13, 5
	v_mfma_scale_f32_32x32x64_f8f6f4 v[96:111], v[148:151], v[134:139], v[96:111], v177, v172 op_sel_hi:[0,0,0] cbsz:4 blgp:2
	s_cselect_b32 s13, s34, 0
	buffer_load_dwordx4 v200, s[4:7], s42 offen lds
	s_add_i32 m0, s43, 0x3000
	s_add_i32 s42, s33, 0xffffc000
	v_mfma_scale_f32_32x32x64_f8f6f4 v[32:47], v[148:151], v[128:133], v[32:47], v177, v173 op_sel_hi:[0,0,0] cbsz:4 blgp:2
	buffer_load_dwordx4 v200, s[4:7], s42 offen lds
	s_add_i32 m0, s43, 0x4000
	s_add_i32 s42, s33, 0xffffd000
	v_add_u32_e32 v148, s35, v202
	v_add_u32_e32 v149, s35, v198
	ds_read_b128 v[156:159], v148
	ds_read_b128 v[162:165], v148 offset:1536
	v_mfma_scale_f32_32x32x64_f8f6f4 v[80:95], v[144:147], v[134:139], v[80:95], v174, v172 op_sel_hi:[0,0,0] cbsz:4 blgp:2
	buffer_load_dwordx4 v200, s[4:7], s42 offen lds
	v_mfma_scale_f32_32x32x64_f8f6f4 v[16:31], v[144:147], v[128:133], v[16:31], v174, v173 op_sel_hi:[0,0,0] cbsz:4 blgp:2
	v_add_u32_e32 v144, s35, v199
	ds_read_b64 v[160:161], v149
	ds_read_b64 v[166:167], v144
	ds_read_b128 v[144:147], v152
	ds_read_b128 v[148:151], v152 offset:1024
	v_mfma_scale_f32_32x32x64_f8f6f4 v[64:79], v[140:143], v[134:139], v[64:79], v175, v172 op_sel_hi:[0,0,0] cbsz:4 blgp:2
	ds_read_b128 v[134:137], v152 offset:2048
	ds_read_b128 v[188:191], v152 offset:3072
	v_mfma_scale_f32_32x32x64_f8f6f4 v[0:15], v[140:143], v[128:133], v[0:15], v175, v173 op_sel_hi:[0,0,0] cbsz:4 blgp:2
	s_mul_i32 s34, s30, 0x5000
	s_waitcnt vmcnt(15)
	s_add_i32 s43, s21, s34
	s_add_i32 s42, s31, 0xfffff000
	s_mov_b32 m0, s43
	s_waitcnt lgkmcnt(0)
	v_mfma_scale_f32_32x32x64_f8f6f4 v[112:127], v[144:147], v[156:161], v[112:127], v176, v172 op_sel_hi:[0,0,0] cbsz:4 blgp:2
	buffer_load_dwordx4 v200, s[4:7], s42 offen lds
	s_add_i32 m0, s43, 0x1000
	s_nop 0
	v_mfma_scale_f32_32x32x64_f8f6f4 v[48:63], v[144:147], v[162:167], v[48:63], v176, v173 op_sel_hi:[0,0,0] cbsz:4 blgp:2
	buffer_load_dwordx4 v200, s[4:7], s31 offen lds
	s_add_i32 m0, s43, 0x2000
	s_add_i32 s42, s33, 0xffffe000
	s_mul_i32 s35, s13, 0x5000
	v_add_u32_e32 v128, s35, v202
	v_add_u32_e32 v132, s35, v198
	v_add_u32_e32 v133, s35, v199
	v_add_u32_e32 v140, s35, v201
	v_mfma_scale_f32_32x32x64_f8f6f4 v[96:111], v[148:151], v[156:161], v[96:111], v177, v172 op_sel_hi:[0,0,0] cbsz:4 blgp:2
	buffer_load_dwordx4 v200, s[4:7], s42 offen lds
	s_add_i32 m0, s43, 0x3000
	s_add_i32 s42, s33, 0xfffff000
	s_add_i32 s34, s30, 1
	s_cmp_lg_u32 s30, 5
	s_cselect_b32 s30, s34, 0
	s_add_i32 s34, s13, 1
	s_cmp_lg_u32 s13, 5
	s_cselect_b32 s13, s34, 0
	v_mfma_scale_f32_32x32x64_f8f6f4 v[32:47], v[148:151], v[162:167], v[32:47], v177, v173 op_sel_hi:[0,0,0] cbsz:4 blgp:2
	buffer_load_dwordx4 v200, s[4:7], s42 offen lds
	s_add_i32 m0, s43, 0x4000
	s_nop 0
	v_mfma_scale_f32_32x32x64_f8f6f4 v[80:95], v[134:137], v[156:161], v[80:95], v174, v172 op_sel_hi:[0,0,0] cbsz:4 blgp:2
	buffer_load_dwordx4 v200, s[4:7], s33 offen lds
	v_mfma_scale_f32_32x32x64_f8f6f4 v[16:31], v[134:137], v[162:167], v[16:31], v174, v173 op_sel_hi:[0,0,0] cbsz:4 blgp:2
	ds_read_b128 v[134:137], v128
	ds_read_b128 v[128:131], v128 offset:1536
	ds_read_b64 v[138:139], v132
	ds_read_b64 v[132:133], v133
	ds_read_b128 v[152:155], v140
	ds_read_b128 v[148:151], v140 offset:1024
	ds_read_b128 v[144:147], v140 offset:2048
	ds_read_b128 v[140:143], v140 offset:3072
	v_mfma_scale_f32_32x32x64_f8f6f4 v[64:79], v[188:191], v[156:161], v[64:79], v175, v172 op_sel_hi:[0,0,0] cbsz:4 blgp:2
	v_mfma_scale_f32_32x32x64_f8f6f4 v[0:15], v[188:191], v[162:167], v[0:15], v175, v173 op_sel_hi:[0,0,0] cbsz:4 blgp:2
	s_add_i32 s12, s12, 2
	s_addk_i32 s31, 0x4000
	s_addk_i32 s33, 0x6000
	s_cmp_gt_u32 s12, 23
	s_cbranch_scc0 .LBB1_34
	s_mul_i32 s12, s30, 0x5000
	s_waitcnt vmcnt(10)
	s_add_i32 s12, s21, s12
	s_waitcnt lgkmcnt(0)
	s_barrier
	s_add_i32 s31, s27, 0x3e000
	s_mov_b32 m0, s12
	s_add_i32 s27, s27, 0x3f000
	buffer_load_dwordx4 v200, s[4:7], s31 offen lds
	s_add_i32 m0, s12, 0x1000
	s_waitcnt lgkmcnt(0)
	v_mfma_scale_f32_32x32x64_f8f6f4 v[112:127], v[152:155], v[134:139], v[112:127], v176, v172 op_sel_hi:[0,0,0] cbsz:4 blgp:2
	buffer_load_dwordx4 v200, s[4:7], s27 offen lds
	s_add_i32 m0, s12, 0x2000
	s_add_i32 s27, s23, 0x5d000
	buffer_load_dwordx4 v200, s[4:7], s27 offen lds
	s_add_i32 m0, s12, 0x3000
	s_add_i32 s27, s23, 0x5e000
	buffer_load_dwordx4 v200, s[4:7], s27 offen lds
	s_add_i32 m0, s12, 0x4000
	s_add_i32 s12, s23, 0x5f000
	buffer_load_dwordx4 v200, s[4:7], s12 offen lds
	v_mfma_scale_f32_32x32x64_f8f6f4 v[48:63], v[152:155], v[128:133], v[48:63], v176, v173 op_sel_hi:[0,0,0] cbsz:4 blgp:2
	s_mul_i32 s31, s13, 0x5000
	s_lshl_b32 s12, s2, 18
	v_add_u32_e32 v154, s31, v199
	v_add_u32_e32 v164, s31, v201
	s_or_b32 s27, s12, s21
	s_add_i32 s12, s30, 1
	s_mul_i32 s23, s29, 0x60000
	v_mfma_scale_f32_32x32x64_f8f6f4 v[96:111], v[148:151], v[134:139], v[96:111], v177, v172 op_sel_hi:[0,0,0] cbsz:4 blgp:2
	s_cmp_lg_u32 s30, 5
	s_cselect_b32 s33, s12, 0
	s_add_i32 s12, s13, 1
	s_add_i32 s23, s23, s16
	s_cmp_lg_u32 s13, 5
	s_cselect_b32 s34, s12, 0
	v_mfma_scale_f32_32x32x64_f8f6f4 v[32:47], v[148:151], v[128:133], v[32:47], v177, v173 op_sel_hi:[0,0,0] cbsz:4 blgp:2
	v_add_u32_e32 v148, s31, v202
	v_add_u32_e32 v149, s31, v198
	v_mfma_scale_f32_32x32x64_f8f6f4 v[80:95], v[144:147], v[134:139], v[80:95], v174, v172 op_sel_hi:[0,0,0] cbsz:4 blgp:2
	v_mfma_scale_f32_32x32x64_f8f6f4 v[16:31], v[144:147], v[128:133], v[16:31], v174, v173 op_sel_hi:[0,0,0] cbsz:4 blgp:2
	ds_read_b128 v[144:147], v148
	ds_read_b128 v[150:153], v148 offset:1536
	ds_read_b64 v[148:149], v149
	ds_read_b64 v[154:155], v154
	ds_read_b128 v[156:159], v164
	ds_read_b128 v[160:163], v164 offset:1024
	v_mfma_scale_f32_32x32x64_f8f6f4 v[64:79], v[140:143], v[134:139], v[64:79], v175, v172 op_sel_hi:[0,0,0] cbsz:4 blgp:2
	ds_read_b128 v[134:137], v164 offset:2048
	ds_read_b128 v[164:167], v164 offset:3072
	v_mfma_scale_f32_32x32x64_f8f6f4 v[0:15], v[140:143], v[128:133], v[0:15], v175, v173 op_sel_hi:[0,0,0] cbsz:4 blgp:2
	s_mul_i32 s12, s33, 0x5000
	s_waitcnt vmcnt(15)
	s_add_i32 s12, s21, s12
	s_mov_b32 m0, s12
	s_or_b32 s13, s27, 0x1000
	buffer_load_dwordx4 v200, s[4:7], s27 offen lds
	s_add_i32 m0, s12, 0x1000
	s_waitcnt lgkmcnt(0)
	v_mfma_scale_f32_32x32x64_f8f6f4 v[112:127], v[156:159], v[144:149], v[112:127], v176, v172 op_sel_hi:[0,0,0] cbsz:4 blgp:2
	buffer_load_dwordx4 v200, s[4:7], s13 offen lds
	s_add_i32 m0, s12, 0x2000
	s_or_b32 s13, s23, 0x1000
	buffer_load_dwordx4 v200, s[4:7], s23 offen lds
	s_add_i32 m0, s12, 0x3000
	s_nop 0
	buffer_load_dwordx4 v200, s[4:7], s13 offen lds
	s_add_i32 m0, s12, 0x4000
	s_or_b32 s12, s23, 0x2000
	buffer_load_dwordx4 v200, s[4:7], s12 offen lds
	s_lshl_b32 s12, s2, 8
	s_lshl_b32 s2, s28, 11
	s_and_b32 s2, s2, 0x800
	s_or_b32 s31, s2, 0x1e000
	s_ashr_i32 s13, s12, 31
	s_add_i32 s30, s31, s22
	v_lshl_add_u64 v[128:129], s[12:13], 2, v[170:171]
	s_mov_b32 m0, s30
	v_mfma_scale_f32_32x32x64_f8f6f4 v[48:63], v[156:159], v[150:155], v[48:63], v176, v173 op_sel_hi:[0,0,0] cbsz:4 blgp:2
	global_load_lds_dword v[128:129], off
	s_mul_i32 s12, s34, 0x5000
	v_add_u32_e32 v132, s12, v202
	v_add_u32_e32 v133, s12, v198
	v_add_u32_e32 v138, s12, v199
	s_add_i32 s2, s33, 1
	v_mfma_scale_f32_32x32x64_f8f6f4 v[96:111], v[160:163], v[144:149], v[96:111], v177, v172 op_sel_hi:[0,0,0] cbsz:4 blgp:2
	s_cmp_lg_u32 s33, 5
	s_cselect_b32 s2, s2, 0
	v_mfma_scale_f32_32x32x64_f8f6f4 v[32:47], v[160:163], v[150:155], v[32:47], v177, v173 op_sel_hi:[0,0,0] cbsz:4 blgp:2
	v_add_u32_e32 v160, s12, v201
	s_add_i32 s12, s34, 1
	s_cmp_lg_u32 s34, 5
	s_cselect_b32 s12, s12, 0
	v_mfma_scale_f32_32x32x64_f8f6f4 v[80:95], v[134:137], v[144:149], v[80:95], v174, v172 op_sel_hi:[0,0,0] cbsz:4 blgp:2
	v_mfma_scale_f32_32x32x64_f8f6f4 v[16:31], v[134:137], v[150:155], v[16:31], v174, v173 op_sel_hi:[0,0,0] cbsz:4 blgp:2
	ds_read_b128 v[128:131], v132
	ds_read_b128 v[134:137], v132 offset:1536
	ds_read_b64 v[132:133], v133
	ds_read_b64 v[138:139], v138
	ds_read_b128 v[140:143], v160
	ds_read_b128 v[156:159], v160 offset:1024
	v_mfma_scale_f32_32x32x64_f8f6f4 v[64:79], v[164:167], v[144:149], v[64:79], v175, v172 op_sel_hi:[0,0,0] cbsz:4 blgp:2
	ds_read_b128 v[144:147], v160 offset:2048
	ds_read_b128 v[160:163], v160 offset:3072
	v_mfma_scale_f32_32x32x64_f8f6f4 v[0:15], v[164:167], v[150:155], v[0:15], v175, v173 op_sel_hi:[0,0,0] cbsz:4 blgp:2
	s_mul_i32 s13, s2, 0x5000
	s_waitcnt vmcnt(10)
	s_add_i32 s13, s21, s13
	s_waitcnt lgkmcnt(0)
	s_barrier
	s_or_b32 s33, s27, 0x2000
	s_mov_b32 m0, s13
	s_waitcnt lgkmcnt(0)
	v_mfma_scale_f32_32x32x64_f8f6f4 v[112:127], v[140:143], v[128:133], v[112:127], v176, v172 op_sel_hi:[0,0,0] cbsz:4 blgp:2
	buffer_load_dwordx4 v200, s[4:7], s33 offen lds
	s_add_i32 m0, s13, 0x1000
	s_or_b32 s33, s27, 0x3000
	buffer_load_dwordx4 v200, s[4:7], s33 offen lds
	s_add_i32 m0, s13, 0x2000
	s_or_b32 s33, s23, 0x3000
	buffer_load_dwordx4 v200, s[4:7], s33 offen lds
	s_add_i32 m0, s13, 0x3000
	s_or_b32 s33, s23, 0x4000
	buffer_load_dwordx4 v200, s[4:7], s33 offen lds
	s_add_i32 m0, s13, 0x4000
	s_or_b32 s13, s23, 0x5000
	buffer_load_dwordx4 v200, s[4:7], s13 offen lds
	v_mfma_scale_f32_32x32x64_f8f6f4 v[48:63], v[140:143], v[134:139], v[48:63], v176, v173 op_sel_hi:[0,0,0] cbsz:4 blgp:2
	s_mul_i32 s33, s12, 0x5000
	v_add_u32_e32 v148, s33, v202
	v_add_u32_e32 v150, s33, v198
	v_add_u32_e32 v151, s33, v199
	v_add_u32_e32 v164, s33, v201
	s_add_i32 s13, s2, 1
	s_cmp_lg_u32 s2, 5
	v_mfma_scale_f32_32x32x64_f8f6f4 v[96:111], v[156:159], v[128:133], v[96:111], v177, v172 op_sel_hi:[0,0,0] cbsz:4 blgp:2
	s_cselect_b32 s2, s13, 0
	s_add_i32 s13, s12, 1
	s_cmp_lg_u32 s12, 5
	s_cselect_b32 s12, s13, 0
	v_mfma_scale_f32_32x32x64_f8f6f4 v[32:47], v[156:159], v[134:139], v[32:47], v177, v173 op_sel_hi:[0,0,0] cbsz:4 blgp:2
	v_mfma_scale_f32_32x32x64_f8f6f4 v[80:95], v[144:147], v[128:133], v[80:95], v174, v172 op_sel_hi:[0,0,0] cbsz:4 blgp:2
	v_mfma_scale_f32_32x32x64_f8f6f4 v[16:31], v[144:147], v[134:139], v[16:31], v174, v173 op_sel_hi:[0,0,0] cbsz:4 blgp:2
	ds_read_b128 v[140:143], v148
	ds_read_b128 v[146:149], v148 offset:1536
	ds_read_b64 v[144:145], v150
	ds_read_b64 v[150:151], v151
	ds_read_b128 v[152:155], v164
	ds_read_b128 v[156:159], v164 offset:1024
	v_mfma_scale_f32_32x32x64_f8f6f4 v[64:79], v[160:163], v[128:133], v[64:79], v175, v172 op_sel_hi:[0,0,0] cbsz:4 blgp:2
	ds_read_b128 v[128:131], v164 offset:2048
	ds_read_b128 v[164:167], v164 offset:3072
	v_mfma_scale_f32_32x32x64_f8f6f4 v[0:15], v[160:163], v[134:139], v[0:15], v175, v173 op_sel_hi:[0,0,0] cbsz:4 blgp:2
	s_mul_i32 s13, s2, 0x5000
	s_waitcnt vmcnt(15)
	s_add_i32 s13, s21, s13
	s_or_b32 s33, s27, 0x4000
	s_mov_b32 m0, s13
	s_waitcnt lgkmcnt(0)
	v_mfma_scale_f32_32x32x64_f8f6f4 v[112:127], v[152:155], v[140:145], v[112:127], v176, v172 op_sel_hi:[0,0,0] cbsz:4 blgp:2
	buffer_load_dwordx4 v200, s[4:7], s33 offen lds
	s_add_i32 m0, s13, 0x1000
	s_or_b32 s33, s27, 0x5000
	buffer_load_dwordx4 v200, s[4:7], s33 offen lds
	s_add_i32 m0, s13, 0x2000
	s_or_b32 s33, s23, 0x6000
	buffer_load_dwordx4 v200, s[4:7], s33 offen lds
	s_add_i32 m0, s13, 0x3000
	s_or_b32 s33, s23, 0x7000
	buffer_load_dwordx4 v200, s[4:7], s33 offen lds
	s_add_i32 m0, s13, 0x4000
	s_or_b32 s13, s23, 0x8000
	buffer_load_dwordx4 v200, s[4:7], s13 offen lds
	v_mfma_scale_f32_32x32x64_f8f6f4 v[48:63], v[152:155], v[146:151], v[48:63], v176, v173 op_sel_hi:[0,0,0] cbsz:4 blgp:2
	s_mul_i32 s33, s12, 0x5000
	v_add_u32_e32 v132, s33, v202
	v_add_u32_e32 v133, s33, v198
	v_add_u32_e32 v138, s33, v199
	v_add_u32_e32 v160, s33, v201
	s_add_i32 s13, s2, 1
	s_cmp_lg_u32 s2, 5
	v_mfma_scale_f32_32x32x64_f8f6f4 v[96:111], v[156:159], v[140:145], v[96:111], v177, v172 op_sel_hi:[0,0,0] cbsz:4 blgp:2
	s_cselect_b32 s2, s13, 0
	s_add_i32 s13, s12, 1
	s_cmp_lg_u32 s12, 5
	s_cselect_b32 s33, s13, 0
	v_mfma_scale_f32_32x32x64_f8f6f4 v[32:47], v[156:159], v[146:151], v[32:47], v177, v173 op_sel_hi:[0,0,0] cbsz:4 blgp:2
	v_mfma_scale_f32_32x32x64_f8f6f4 v[80:95], v[128:131], v[140:145], v[80:95], v174, v172 op_sel_hi:[0,0,0] cbsz:4 blgp:2
	v_mfma_scale_f32_32x32x64_f8f6f4 v[16:31], v[128:131], v[146:151], v[16:31], v174, v173 op_sel_hi:[0,0,0] cbsz:4 blgp:2
	ds_read_b128 v[128:131], v132
	ds_read_b128 v[134:137], v132 offset:1536
	ds_read_b64 v[132:133], v133
	ds_read_b64 v[138:139], v138
	ds_read_b128 v[152:155], v160
	ds_read_b128 v[156:159], v160 offset:1024
	v_mfma_scale_f32_32x32x64_f8f6f4 v[64:79], v[164:167], v[140:145], v[64:79], v175, v172 op_sel_hi:[0,0,0] cbsz:4 blgp:2
	ds_read_b128 v[140:143], v160 offset:2048
	ds_read_b128 v[160:163], v160 offset:3072
	v_mfma_scale_f32_32x32x64_f8f6f4 v[0:15], v[164:167], v[146:151], v[0:15], v175, v173 op_sel_hi:[0,0,0] cbsz:4 blgp:2
	s_mul_i32 s12, s2, 0x5000
	s_waitcnt vmcnt(10)
	s_add_i32 s12, s21, s12
	s_waitcnt lgkmcnt(0)
	s_barrier
	s_or_b32 s13, s27, 0x6000
	s_mov_b32 m0, s12
	s_waitcnt lgkmcnt(0)
	v_mfma_scale_f32_32x32x64_f8f6f4 v[112:127], v[152:155], v[128:133], v[112:127], v176, v172 op_sel_hi:[0,0,0] cbsz:4 blgp:2
	buffer_load_dwordx4 v200, s[4:7], s13 offen lds
	s_add_i32 m0, s12, 0x1000
	s_or_b32 s13, s27, 0x7000
	buffer_load_dwordx4 v200, s[4:7], s13 offen lds
	s_add_i32 m0, s12, 0x2000
	s_or_b32 s13, s23, 0x9000
	buffer_load_dwordx4 v200, s[4:7], s13 offen lds
	s_add_i32 m0, s12, 0x3000
	s_or_b32 s13, s23, 0xa000
	buffer_load_dwordx4 v200, s[4:7], s13 offen lds
	s_add_i32 m0, s12, 0x4000
	s_or_b32 s12, s23, 0xb000
	buffer_load_dwordx4 v200, s[4:7], s12 offen lds
	s_mul_i32 s13, s33, 0x5000
	v_mfma_scale_f32_32x32x64_f8f6f4 v[48:63], v[152:155], v[134:139], v[48:63], v176, v173 op_sel_hi:[0,0,0] cbsz:4 blgp:2
	v_add_u32_e32 v144, s13, v202
	v_add_u32_e32 v145, s13, v198
	v_add_u32_e32 v150, s13, v199
	s_add_i32 s12, s2, 1
	s_cmp_lg_u32 s2, 5
	s_cselect_b32 s34, s12, 0
	v_mfma_scale_f32_32x32x64_f8f6f4 v[96:111], v[156:159], v[128:133], v[96:111], v177, v172 op_sel_hi:[0,0,0] cbsz:4 blgp:2
	v_mfma_scale_f32_32x32x64_f8f6f4 v[32:47], v[156:159], v[134:139], v[32:47], v177, v173 op_sel_hi:[0,0,0] cbsz:4 blgp:2
	v_mfma_scale_f32_32x32x64_f8f6f4 v[80:95], v[140:143], v[128:133], v[80:95], v174, v172 op_sel_hi:[0,0,0] cbsz:4 blgp:2
	v_mfma_scale_f32_32x32x64_f8f6f4 v[16:31], v[140:143], v[134:139], v[16:31], v174, v173 op_sel_hi:[0,0,0] cbsz:4 blgp:2
	ds_read_b128 v[140:143], v144
	ds_read_b128 v[146:149], v144 offset:1536
	ds_read_b64 v[144:145], v145
	ds_read_b64 v[150:151], v150
	v_mfma_scale_f32_32x32x64_f8f6f4 v[64:79], v[160:163], v[128:133], v[64:79], v175, v172 op_sel_hi:[0,0,0] cbsz:4 blgp:2
	v_add_u32_e32 v132, s13, v201
	ds_read_b128 v[128:131], v132
	ds_read_b128 v[152:155], v132 offset:1024
	ds_read_b128 v[156:159], v132 offset:2048
	ds_read_b128 v[164:167], v132 offset:3072
	v_mfma_scale_f32_32x32x64_f8f6f4 v[0:15], v[160:163], v[134:139], v[0:15], v175, v173 op_sel_hi:[0,0,0] cbsz:4 blgp:2
	s_mul_i32 s2, s34, 0x5000
	s_waitcnt vmcnt(15)
	s_add_i32 s2, s21, s2
	s_or_b32 s12, s27, 0x8000
	s_mov_b32 m0, s2
	s_waitcnt lgkmcnt(0)
	v_mfma_scale_f32_32x32x64_f8f6f4 v[112:127], v[128:131], v[140:145], v[112:127], v176, v172 op_sel_hi:[0,0,0] cbsz:4 blgp:2
	buffer_load_dwordx4 v200, s[4:7], s12 offen lds
	s_add_i32 m0, s2, 0x1000
	s_or_b32 s12, s27, 0x9000
	buffer_load_dwordx4 v200, s[4:7], s12 offen lds
	s_add_i32 m0, s2, 0x2000
	s_or_b32 s12, s23, 0xc000
	buffer_load_dwordx4 v200, s[4:7], s12 offen lds
	s_add_i32 m0, s2, 0x3000
	s_or_b32 s12, s23, 0xd000
	buffer_load_dwordx4 v200, s[4:7], s12 offen lds
	s_add_i32 m0, s2, 0x4000
	s_or_b32 s2, s23, 0xe000
	buffer_load_dwordx4 v200, s[4:7], s2 offen lds
	v_mfma_scale_f32_32x32x64_f8f6f4 v[48:63], v[128:131], v[146:151], v[48:63], v176, v173 op_sel_hi:[0,0,0] cbsz:4 blgp:2
	v_mfma_scale_f32_32x32x64_f8f6f4 v[96:111], v[152:155], v[140:145], v[96:111], v177, v172 op_sel_hi:[0,0,0] cbsz:4 blgp:2
	v_mfma_scale_f32_32x32x64_f8f6f4 v[32:47], v[152:155], v[146:151], v[32:47], v177, v173 op_sel_hi:[0,0,0] cbsz:4 blgp:2
	v_mfma_scale_f32_32x32x64_f8f6f4 v[80:95], v[156:159], v[140:145], v[80:95], v174, v172 op_sel_hi:[0,0,0] cbsz:4 blgp:2
	v_mfma_scale_f32_32x32x64_f8f6f4 v[16:31], v[156:159], v[146:151], v[16:31], v174, v173 op_sel_hi:[0,0,0] cbsz:4 blgp:2
	v_mfma_scale_f32_32x32x64_f8f6f4 v[64:79], v[164:167], v[140:145], v[64:79], v175, v172 op_sel_hi:[0,0,0] cbsz:4 blgp:2
	v_mfma_scale_f32_32x32x64_f8f6f4 v[0:15], v[164:167], v[146:151], v[0:15], v175, v173 op_sel_hi:[0,0,0] cbsz:4 blgp:2
	s_cmp_gt_u32 s74, 8
	s_cbranch_scc1 .Lge_skip_b
	v_fmac_f32_e32 v244, v228, v236
	v_fmac_f32_e32 v244, v229, v237
	v_fmac_f32_e32 v244, v230, v238
	v_fmac_f32_e32 v244, v231, v239
	v_fmac_f32_e32 v244, v232, v240
	v_fmac_f32_e32 v244, v233, v241
	v_fmac_f32_e32 v244, v234, v242
	v_fmac_f32_e32 v244, v235, v243
	s_and_b32 s75, s74, 3
	s_cmp_lg_u32 s75, 0
	s_cbranch_scc1 .Lge_issue_b
	s_nop 1
	v_add_f32_dpp v244, v244, v244 quad_perm:[1,0,3,2] row_mask:0xf bank_mask:0xf
	s_nop 1
	v_add_f32_dpp v244, v244, v244 quad_perm:[2,3,0,1] row_mask:0xf bank_mask:0xf
	s_nop 1
	v_add_f32_dpp v244, v244, v244 row_half_mirror row_mask:0xf bank_mask:0xf
	s_nop 1
	v_add_f32_dpp v244, v244, v244 row_mirror row_mask:0xf bank_mask:0xf
	s_nop 1
	v_add_f32_dpp v244, v244, v244 row_bcast:15 row_mask:0xa bank_mask:0xf
	s_nop 1
	v_add_f32_dpp v244, v244, v244 row_bcast:31 row_mask:0xc bank_mask:0xf
	s_nop 1
	v_readlane_b32 s75, v244, 63
	v_mov_b32_e32 v247, 0
	s_mov_b64 s[80:81], exec
	s_nop 1
	v_mov_b32_e32 v246, s75
	s_mov_b64 exec, 1
	global_store_dword v247, v246, s[62:63]
	s_mov_b64 exec, s[80:81]
	s_add_u32 s62, s62, 4
	s_addc_u32 s63, s63, 0
	v_mov_b32_e32 v244, 0
	s_cmp_eq_u32 s74, 8
	s_cbranch_scc1 .Lge_done_b
	s_max_i32 s75, s77, 0
	s_min_i32 s75, s75, 0x7cff
	s_lshl_b32 s82, s75, 13
	s_add_u32 s84, s66, s82
	s_addc_u32 s85, s67, 0
	s_add_u32 s72, s72, 1
	s_lshl_b32 s82, s72, 13
	s_add_u32 s86, s64, s82
	s_addc_u32 s87, s65, 0

.Lge_skip_b:
	s_nop 0
	v_exp_f32_e32 v128, v112
	v_exp_f32_e32 v130, v113
	s_nop 2
	v_exp_f32_e32 v129, v48
	v_exp_f32_e32 v131, v49
	v_exp_f32_e32 v132, v114
	v_exp_f32_e32 v134, v115
	v_exp_f32_e32 v133, v50
	v_exp_f32_e32 v135, v51
	v_exp_f32_e32 v136, v116
	v_exp_f32_e32 v138, v117
	v_exp_f32_e32 v137, v52
	v_exp_f32_e32 v139, v53
	v_exp_f32_e32 v140, v118
	v_exp_f32_e32 v142, v119
	v_exp_f32_e32 v141, v54
	v_exp_f32_e32 v143, v55
	v_pk_add_f32 v[128:129], v[128:129], 0 op_sel_hi:[1,0]
	v_pk_add_f32 v[130:131], v[130:131], 0 op_sel_hi:[1,0]
	v_exp_f32_e32 v144, v120
	v_exp_f32_e32 v146, v121
	v_exp_f32_e32 v145, v56
	v_exp_f32_e32 v147, v57
	v_exp_f32_e32 v148, v122
	v_exp_f32_e32 v150, v123
	v_exp_f32_e32 v149, v58
	v_exp_f32_e32 v151, v59
	v_pk_add_f32 v[128:129], v[132:133], v[128:129]
	v_pk_add_f32 v[130:131], v[134:135], v[130:131]
	v_exp_f32_e32 v152, v124
	v_exp_f32_e32 v154, v125
	v_exp_f32_e32 v153, v60
	v_exp_f32_e32 v155, v61
	v_pk_add_f32 v[128:129], v[136:137], v[128:129]
	v_pk_add_f32 v[130:131], v[138:139], v[130:131]
	v_exp_f32_e32 v156, v126
	v_exp_f32_e32 v158, v127
	v_exp_f32_e32 v157, v62
	v_exp_f32_e32 v159, v63
	v_pk_add_f32 v[128:129], v[140:141], v[128:129]
	v_pk_add_f32 v[130:131], v[142:143], v[130:131]
	v_exp_f32_e32 v160, v96
	v_exp_f32_e32 v162, v97
	v_exp_f32_e32 v161, v32
	v_exp_f32_e32 v163, v33
	v_pk_add_f32 v[128:129], v[144:145], v[128:129]
	v_pk_add_f32 v[130:131], v[146:147], v[130:131]
	v_exp_f32_e32 v164, v98
	v_exp_f32_e32 v166, v99
	v_exp_f32_e32 v165, v34
	v_exp_f32_e32 v167, v35
	v_pk_add_f32 v[128:129], v[148:149], v[128:129]
	v_pk_add_f32 v[130:131], v[150:151], v[130:131]
	v_exp_f32_e32 v172, v100
	v_exp_f32_e32 v174, v101
	v_exp_f32_e32 v173, v36
	v_exp_f32_e32 v175, v37
	v_pk_add_f32 v[128:129], v[152:153], v[128:129]
	v_pk_add_f32 v[130:131], v[154:155], v[130:131]
	v_exp_f32_e32 v176, v102
	v_exp_f32_e32 v182, v103
	v_exp_f32_e32 v177, v38
	v_pk_add_f32 v[128:129], v[156:157], v[128:129]
	v_exp_f32_e32 v183, v39
	v_pk_add_f32 v[130:131], v[158:159], v[130:131]
	v_pk_add_f32 v[128:129], v[160:161], v[128:129]
	v_pk_add_f32 v[130:131], v[162:163], v[130:131]
	v_exp_f32_e32 v132, v104
	v_exp_f32_e32 v134, v105
	v_exp_f32_e32 v133, v40
	v_exp_f32_e32 v135, v41
	v_pk_add_f32 v[128:129], v[164:165], v[128:129]
	v_pk_add_f32 v[130:131], v[166:167], v[130:131]
	v_exp_f32_e32 v136, v106
	v_exp_f32_e32 v138, v107
	v_exp_f32_e32 v137, v42
	v_exp_f32_e32 v139, v43
	v_pk_add_f32 v[128:129], v[172:173], v[128:129]
	v_pk_add_f32 v[130:131], v[174:175], v[130:131]
	v_exp_f32_e32 v140, v108
	v_exp_f32_e32 v142, v109
	v_exp_f32_e32 v141, v44
	v_exp_f32_e32 v143, v45
	v_pk_add_f32 v[128:129], v[176:177], v[128:129]
	v_pk_add_f32 v[130:131], v[182:183], v[130:131]
	v_exp_f32_e32 v144, v110
	v_exp_f32_e32 v146, v111
	v_exp_f32_e32 v145, v46
	v_exp_f32_e32 v147, v47
	v_exp_f32_e32 v148, v80
	v_exp_f32_e32 v150, v81
	v_exp_f32_e32 v149, v16
	v_exp_f32_e32 v151, v17
	v_pk_add_f32 v[128:129], v[132:133], v[128:129]
	v_pk_add_f32 v[130:131], v[134:135], v[130:131]
	v_exp_f32_e32 v152, v82
	v_exp_f32_e32 v154, v83
	v_exp_f32_e32 v153, v18
	v_exp_f32_e32 v155, v19
	v_pk_add_f32 v[128:129], v[136:137], v[128:129]
	v_pk_add_f32 v[130:131], v[138:139], v[130:131]
	v_exp_f32_e32 v156, v84
	v_exp_f32_e32 v158, v85
	v_exp_f32_e32 v157, v20
	v_exp_f32_e32 v159, v21
	v_pk_add_f32 v[128:129], v[140:141], v[128:129]
	v_pk_add_f32 v[130:131], v[142:143], v[130:131]
	v_exp_f32_e32 v160, v86
	v_exp_f32_e32 v162, v87
	v_exp_f32_e32 v161, v22
	v_exp_f32_e32 v163, v23
	v_pk_add_f32 v[128:129], v[144:145], v[128:129]
	v_pk_add_f32 v[130:131], v[146:147], v[130:131]
	v_exp_f32_e32 v164, v88
	v_exp_f32_e32 v166, v89
	v_exp_f32_e32 v165, v24
	v_exp_f32_e32 v167, v25
	v_pk_add_f32 v[128:129], v[148:149], v[128:129]
	v_pk_add_f32 v[130:131], v[150:151], v[130:131]
	v_exp_f32_e32 v172, v90
	v_exp_f32_e32 v174, v91
	v_exp_f32_e32 v173, v26
	v_exp_f32_e32 v175, v27
	v_pk_add_f32 v[128:129], v[152:153], v[128:129]
	v_pk_add_f32 v[130:131], v[154:155], v[130:131]
	v_exp_f32_e32 v176, v92
	v_exp_f32_e32 v182, v93
	v_exp_f32_e32 v177, v28
	v_pk_add_f32 v[128:129], v[156:157], v[128:129]
	v_exp_f32_e32 v183, v29
	v_pk_add_f32 v[130:131], v[158:159], v[130:131]
	v_pk_add_f32 v[128:129], v[160:161], v[128:129]
	v_pk_add_f32 v[130:131], v[162:163], v[130:131]
	v_exp_f32_e32 v134, v94
	v_exp_f32_e32 v136, v95
	v_exp_f32_e32 v135, v30
	v_exp_f32_e32 v137, v31
	v_pk_add_f32 v[128:129], v[164:165], v[128:129]
	v_pk_add_f32 v[130:131], v[166:167], v[130:131]
	v_exp_f32_e32 v138, v64
	v_exp_f32_e32 v140, v65
	v_exp_f32_e32 v139, v0
	v_exp_f32_e32 v141, v1
	v_pk_add_f32 v[128:129], v[172:173], v[128:129]
	v_pk_add_f32 v[130:131], v[174:175], v[130:131]
	v_exp_f32_e32 v142, v66
	v_exp_f32_e32 v144, v67
	v_exp_f32_e32 v143, v2
	v_exp_f32_e32 v145, v3
	v_pk_add_f32 v[128:129], v[176:177], v[128:129]
	v_pk_add_f32 v[130:131], v[182:183], v[130:131]
	v_exp_f32_e32 v146, v68
	v_exp_f32_e32 v148, v69
	v_exp_f32_e32 v147, v4
	v_exp_f32_e32 v149, v5
	v_exp_f32_e32 v150, v70
	v_exp_f32_e32 v152, v71
	v_exp_f32_e32 v151, v6
	v_exp_f32_e32 v153, v7
	v_pk_add_f32 v[128:129], v[134:135], v[128:129]
	v_pk_add_f32 v[130:131], v[136:137], v[130:131]
	v_exp_f32_e32 v154, v72
	v_exp_f32_e32 v156, v73
	v_exp_f32_e32 v155, v8
	v_exp_f32_e32 v157, v9
	v_pk_add_f32 v[128:129], v[138:139], v[128:129]
	v_pk_add_f32 v[130:131], v[140:141], v[130:131]
	v_exp_f32_e32 v158, v74
	v_exp_f32_e32 v160, v75
	v_exp_f32_e32 v159, v10
	v_exp_f32_e32 v161, v11
	v_pk_add_f32 v[128:129], v[142:143], v[128:129]
	v_pk_add_f32 v[130:131], v[144:145], v[130:131]
	v_exp_f32_e32 v162, v76
	v_exp_f32_e32 v164, v77
	v_exp_f32_e32 v163, v12
	v_exp_f32_e32 v165, v13
	v_pk_add_f32 v[128:129], v[146:147], v[128:129]
	v_pk_add_f32 v[130:131], v[148:149], v[130:131]
	v_exp_f32_e32 v166, v78
	v_exp_f32_e32 v172, v79
	v_exp_f32_e32 v167, v14
	v_exp_f32_e32 v173, v15
	v_pk_add_f32 v[128:129], v[150:151], v[128:129]
	v_pk_add_f32 v[130:131], v[152:153], v[130:131]
	v_and_b32_e32 v133, 64, v179
	v_pk_add_f32 v[128:129], v[154:155], v[128:129]
	v_pk_add_f32 v[130:131], v[156:157], v[130:131]
	v_xor_b32_e32 v132, 32, v179
	v_add_u32_e32 v133, 64, v133
	v_pk_add_f32 v[128:129], v[158:159], v[128:129]
	v_pk_add_f32 v[130:131], v[160:161], v[130:131]
	v_cmp_lt_i32_e32 vcc, v132, v133
	v_pk_add_f32 v[128:129], v[162:163], v[128:129]
	v_pk_add_f32 v[130:131], v[164:165], v[130:131]
	v_cndmask_b32_e32 v132, v179, v132, vcc
	v_pk_add_f32 v[128:129], v[166:167], v[128:129]
	v_pk_add_f32 v[130:131], v[172:173], v[130:131]
	v_lshlrev_b32_e32 v132, 2, v132
	v_pk_add_f32 v[128:129], v[128:129], v[130:131]
	ds_bpermute_b32 v130, v132, v128
	ds_bpermute_b32 v131, v132, v129
	s_lshl_b32 s2, s26, 8
	s_or_b32 s2, s2, s15
	s_waitcnt lgkmcnt(0)
	v_pk_add_f32 v[128:129], v[128:129], v[130:131]
	s_nop 0
	v_cmp_nge_f32_e32 vcc, s17, v129
	s_nop 1
	v_cndmask_b32_e64 v130, 0, 1, vcc
	v_cmp_nge_f32_e32 vcc, s17, v128
	v_lshlrev_b16_e32 v130, 1, v130
	s_nop 0
	v_cndmask_b32_e64 v131, 0, 1, vcc
	v_cmp_nle_f32_e32 vcc, s18, v128
	v_bitop3_b16 v130, v131, 3, v130 bitop3:0xc8
	s_nop 0
	v_cndmask_b32_e64 v131, 0, 1, vcc
	v_cmp_nle_f32_e32 vcc, s18, v129
	v_lshlrev_b16_e32 v131, 2, v131
	s_nop 0
	v_cndmask_b32_e64 v133, 0, 1, vcc
	v_lshlrev_b16_e32 v133, 3, v133
	v_or_b32_e32 v131, v133, v131
	v_bitop3_b16 v130, v130, 15, v131 bitop3:0xc8
	v_cmp_ne_u16_e32 vcc, 0, v130
	s_cbranch_vccz .LBB1_41
	v_max_f32_e32 v130, v113, v113
	v_max_f32_e32 v131, v112, v112
	v_max_f32_e32 v130, v131, v130
	v_max3_f32 v130, v130, v114, v115
	v_max3_f32 v130, v130, v116, v117
	v_max3_f32 v130, v130, v118, v119
	v_max3_f32 v130, v130, v120, v121
	v_max3_f32 v130, v130, v122, v123
	v_max3_f32 v130, v130, v124, v125
	v_max3_f32 v130, v130, v126, v127
	v_max3_f32 v130, v130, v96, v97
	v_max3_f32 v130, v130, v98, v99
	v_max3_f32 v130, v130, v100, v101
	v_max3_f32 v130, v130, v102, v103
	v_max3_f32 v130, v130, v104, v105
	v_max3_f32 v130, v130, v106, v107
	v_max3_f32 v130, v130, v108, v109
	v_max3_f32 v130, v130, v110, v111
	v_max3_f32 v130, v130, v80, v81
	v_max3_f32 v130, v130, v82, v83
	v_max3_f32 v130, v130, v84, v85
	v_max3_f32 v130, v130, v86, v87
	v_max3_f32 v130, v130, v88, v89
	v_max3_f32 v130, v130, v90, v91
	v_max3_f32 v130, v130, v92, v93
	v_max3_f32 v130, v130, v94, v95
	v_max3_f32 v130, v130, v64, v65
	v_max3_f32 v130, v130, v66, v67
	v_max3_f32 v130, v130, v68, v69
	v_max3_f32 v130, v130, v70, v71
	v_max3_f32 v130, v130, v72, v73
	v_max3_f32 v130, v130, v74, v75
	v_max3_f32 v130, v130, v76, v77
	v_max3_f32 v130, v130, v78, v79
	ds_bpermute_b32 v131, v132, v130
	s_waitcnt lgkmcnt(0)
	v_max_f32_e32 v131, v131, v131
	v_max_f32_e32 v130, v130, v131
	v_sub_f32_e32 v112, v112, v130
	v_sub_f32_e32 v113, v113, v130
	v_exp_f32_e32 v112, v112
	v_sub_f32_e32 v114, v114, v130
	v_exp_f32_e32 v113, v113
	v_sub_f32_e32 v115, v115, v130
	v_exp_f32_e32 v114, v114
	v_exp_f32_e32 v115, v115
	v_add_f32_e32 v112, 0, v112
	v_add_f32_e32 v112, v113, v112
	v_sub_f32_e32 v113, v116, v130
	v_add_f32_e32 v112, v114, v112
	v_exp_f32_e32 v113, v113
	v_sub_f32_e32 v114, v117, v130
	v_add_f32_e32 v112, v115, v112
	v_exp_f32_e32 v114, v114
	v_sub_f32_e32 v115, v118, v130
	v_exp_f32_e32 v115, v115
	v_sub_f32_e32 v116, v119, v130
	v_exp_f32_e32 v116, v116
	v_add_f32_e32 v112, v113, v112
	v_sub_f32_e32 v113, v120, v130
	v_add_f32_e32 v112, v114, v112
	v_exp_f32_e32 v113, v113
	v_sub_f32_e32 v114, v121, v130
	v_add_f32_e32 v112, v115, v112
	v_exp_f32_e32 v114, v114
	v_sub_f32_e32 v115, v122, v130
	v_add_f32_e32 v112, v116, v112
	v_exp_f32_e32 v115, v115
	v_sub_f32_e32 v116, v123, v130
	v_exp_f32_e32 v116, v116
	v_add_f32_e32 v112, v113, v112
	v_sub_f32_e32 v113, v124, v130
	v_add_f32_e32 v112, v114, v112
	v_exp_f32_e32 v113, v113
	v_sub_f32_e32 v114, v125, v130
	v_add_f32_e32 v112, v115, v112
	v_exp_f32_e32 v114, v114
	v_sub_f32_e32 v115, v126, v130
	v_add_f32_e32 v112, v116, v112
	v_exp_f32_e32 v115, v115
	v_sub_f32_e32 v116, v127, v130
	v_exp_f32_e32 v116, v116
	v_sub_f32_e32 v96, v96, v130
	v_add_f32_e32 v112, v113, v112
	v_exp_f32_e32 v96, v96
	v_sub_f32_e32 v97, v97, v130
	v_add_f32_e32 v112, v114, v112
	v_exp_f32_e32 v97, v97
	v_sub_f32_e32 v98, v98, v130
	v_add_f32_e32 v112, v115, v112
	v_exp_f32_e32 v98, v98
	v_sub_f32_e32 v99, v99, v130
	v_add_f32_e32 v112, v116, v112
	v_exp_f32_e32 v99, v99
	v_add_f32_e32 v96, v96, v112
	v_add_f32_e32 v96, v97, v96
	v_sub_f32_e32 v97, v100, v130
	v_add_f32_e32 v96, v98, v96
	v_exp_f32_e32 v97, v97
	v_sub_f32_e32 v98, v101, v130
	v_add_f32_e32 v96, v99, v96
	v_exp_f32_e32 v98, v98
	v_sub_f32_e32 v99, v102, v130
	v_exp_f32_e32 v99, v99
	v_sub_f32_e32 v100, v103, v130
	v_exp_f32_e32 v100, v100
	v_add_f32_e32 v96, v97, v96
	v_sub_f32_e32 v97, v104, v130
	v_add_f32_e32 v96, v98, v96
	v_exp_f32_e32 v97, v97
	v_sub_f32_e32 v98, v105, v130
	v_add_f32_e32 v96, v99, v96
	v_exp_f32_e32 v98, v98
	v_sub_f32_e32 v99, v106, v130
	v_add_f32_e32 v96, v100, v96
	v_exp_f32_e32 v99, v99
	v_sub_f32_e32 v100, v107, v130
	v_exp_f32_e32 v100, v100
	v_add_f32_e32 v96, v97, v96
	v_sub_f32_e32 v97, v108, v130
	v_add_f32_e32 v96, v98, v96
	v_exp_f32_e32 v97, v97
	v_sub_f32_e32 v98, v109, v130
	v_add_f32_e32 v96, v99, v96
	v_exp_f32_e32 v98, v98
	v_sub_f32_e32 v99, v110, v130
	v_add_f32_e32 v96, v100, v96
	v_exp_f32_e32 v99, v99
	v_sub_f32_e32 v100, v111, v130
	v_exp_f32_e32 v100, v100
	v_sub_f32_e32 v80, v80, v130
	v_add_f32_e32 v96, v97, v96
	v_exp_f32_e32 v80, v80
	v_sub_f32_e32 v81, v81, v130
	v_add_f32_e32 v96, v98, v96
	v_exp_f32_e32 v81, v81
	v_sub_f32_e32 v82, v82, v130
	v_add_f32_e32 v96, v99, v96
	v_exp_f32_e32 v82, v82
	v_sub_f32_e32 v83, v83, v130
	v_add_f32_e32 v96, v100, v96
	v_exp_f32_e32 v83, v83
	v_add_f32_e32 v80, v80, v96
	v_add_f32_e32 v80, v81, v80
	v_sub_f32_e32 v81, v84, v130
	v_add_f32_e32 v80, v82, v80
	v_exp_f32_e32 v81, v81
	v_sub_f32_e32 v82, v85, v130
	v_add_f32_e32 v80, v83, v80
	v_exp_f32_e32 v82, v82
	v_sub_f32_e32 v83, v86, v130
	v_exp_f32_e32 v83, v83
	v_sub_f32_e32 v84, v87, v130
	v_exp_f32_e32 v84, v84
	v_add_f32_e32 v80, v81, v80
	v_sub_f32_e32 v81, v88, v130
	v_add_f32_e32 v80, v82, v80
	v_exp_f32_e32 v81, v81
	v_sub_f32_e32 v82, v89, v130
	v_add_f32_e32 v80, v83, v80
	v_exp_f32_e32 v82, v82
	v_sub_f32_e32 v83, v90, v130
	v_add_f32_e32 v80, v84, v80
	v_exp_f32_e32 v83, v83
	v_sub_f32_e32 v84, v91, v130
	v_exp_f32_e32 v84, v84
	v_add_f32_e32 v80, v81, v80
	v_sub_f32_e32 v81, v92, v130
	v_add_f32_e32 v80, v82, v80
	v_exp_f32_e32 v81, v81
	v_sub_f32_e32 v82, v93, v130
	v_add_f32_e32 v80, v83, v80
	v_exp_f32_e32 v82, v82
	v_sub_f32_e32 v83, v94, v130
	v_add_f32_e32 v80, v84, v80
	v_exp_f32_e32 v83, v83
	v_sub_f32_e32 v84, v95, v130
	v_exp_f32_e32 v84, v84
	v_sub_f32_e32 v64, v64, v130
	v_add_f32_e32 v80, v81, v80
	v_exp_f32_e32 v64, v64
	v_sub_f32_e32 v65, v65, v130
	v_add_f32_e32 v80, v82, v80
	v_exp_f32_e32 v65, v65
	v_sub_f32_e32 v66, v66, v130
	v_add_f32_e32 v80, v83, v80
	v_exp_f32_e32 v66, v66
	v_sub_f32_e32 v67, v67, v130
	v_add_f32_e32 v80, v84, v80
	v_exp_f32_e32 v67, v67
	v_add_f32_e32 v64, v64, v80
	v_add_f32_e32 v64, v65, v64
	v_sub_f32_e32 v65, v68, v130
	v_add_f32_e32 v64, v66, v64
	v_exp_f32_e32 v65, v65
	v_sub_f32_e32 v66, v69, v130
	v_add_f32_e32 v64, v67, v64
	v_exp_f32_e32 v66, v66
	v_sub_f32_e32 v67, v70, v130
	v_exp_f32_e32 v67, v67
	v_sub_f32_e32 v68, v71, v130
	v_exp_f32_e32 v68, v68
	v_add_f32_e32 v64, v65, v64
	v_sub_f32_e32 v65, v72, v130
	v_add_f32_e32 v64, v66, v64
	v_exp_f32_e32 v65, v65
	v_sub_f32_e32 v66, v73, v130
	v_add_f32_e32 v64, v67, v64
	v_exp_f32_e32 v66, v66
	v_sub_f32_e32 v67, v74, v130
	v_add_f32_e32 v64, v68, v64
	v_exp_f32_e32 v67, v67
	v_sub_f32_e32 v68, v75, v130
	v_exp_f32_e32 v68, v68
	v_add_f32_e32 v64, v65, v64
	v_sub_f32_e32 v65, v76, v130
	v_add_f32_e32 v64, v66, v64
	v_exp_f32_e32 v65, v65
	v_sub_f32_e32 v66, v77, v130
	v_add_f32_e32 v64, v67, v64
	v_exp_f32_e32 v66, v66
	v_sub_f32_e32 v67, v78, v130
	v_add_f32_e32 v64, v68, v64
	v_exp_f32_e32 v67, v67
	v_sub_f32_e32 v68, v79, v130
	v_exp_f32_e32 v68, v68
	v_add_f32_e32 v64, v65, v64
	v_add_f32_e32 v64, v66, v64
	v_add_f32_e32 v64, v67, v64
	v_add_f32_e32 v64, v68, v64
	ds_bpermute_b32 v65, v132, v64
	s_and_saveexec_b64 s[12:13], s[0:1]
	s_cbranch_execz .LBB1_38
	v_or_b32_e32 v186, s2, v184
	v_lshl_add_u64 v[66:67], v[186:187], 2, s[8:9]
	global_atomic_add v66, v[66:67], v180, off sc0
	s_waitcnt lgkmcnt(0)
	v_add_f32_e32 v131, v64, v65
	v_mov_b64_e32 v[64:65], s[10:11]
	v_mad_u64_u32 v[64:65], s[36:37], v186, s19, v[64:65]
	s_waitcnt vmcnt(0)
	v_ashrrev_i32_e32 v67, 31, v66
	v_lshl_add_u64 v[64:65], v[66:67], 3, v[64:65]
	global_store_dwordx2 v[64:65], v[130:131], off

.LBB1_43:
	s_waitcnt vmcnt(0)
	s_cmp_gt_u32 s74, 8
	s_cbranch_scc1 .Lge_skip_c
	v_fmac_f32_e32 v244, v228, v236
	v_fmac_f32_e32 v244, v229, v237
	v_fmac_f32_e32 v244, v230, v238
	v_fmac_f32_e32 v244, v231, v239
	v_fmac_f32_e32 v244, v232, v240
	v_fmac_f32_e32 v244, v233, v241
	v_fmac_f32_e32 v244, v234, v242
	v_fmac_f32_e32 v244, v235, v243
	s_and_b32 s75, s74, 3
	s_cmp_lg_u32 s75, 0
	s_cbranch_scc1 .Lge_issue_c
	s_nop 1
	v_add_f32_dpp v244, v244, v244 quad_perm:[1,0,3,2] row_mask:0xf bank_mask:0xf
	s_nop 1
	v_add_f32_dpp v244, v244, v244 quad_perm:[2,3,0,1] row_mask:0xf bank_mask:0xf
	s_nop 1
	v_add_f32_dpp v244, v244, v244 row_half_mirror row_mask:0xf bank_mask:0xf
	s_nop 1
	v_add_f32_dpp v244, v244, v244 row_mirror row_mask:0xf bank_mask:0xf
	s_nop 1
	v_add_f32_dpp v244, v244, v244 row_bcast:15 row_mask:0xa bank_mask:0xf
	s_nop 1
	v_add_f32_dpp v244, v244, v244 row_bcast:31 row_mask:0xc bank_mask:0xf
	s_nop 1
	v_readlane_b32 s75, v244, 63
	v_mov_b32_e32 v247, 0
	s_mov_b64 s[80:81], exec
	s_nop 1
	v_mov_b32_e32 v246, s75
	s_mov_b64 exec, 1
	global_store_dword v247, v246, s[62:63]
	s_mov_b64 exec, s[80:81]
	s_add_u32 s62, s62, 4
	s_addc_u32 s63, s63, 0
	v_mov_b32_e32 v244, 0
	s_cmp_eq_u32 s74, 8
	s_cbranch_scc1 .Lge_done_c
	s_max_i32 s75, s77, 0
	s_min_i32 s75, s75, 0x7cff
	s_lshl_b32 s82, s75, 13
	s_add_u32 s84, s66, s82
	s_addc_u32 s85, s67, 0
	s_add_u32 s72, s72, 1
	s_lshl_b32 s82, s72, 13
	s_add_u32 s86, s64, s82
	s_addc_u32 s87, s65, 0

	.amdhsa_kernel _Z15gemm_lse_kernelPKhS0_PKjS2_PfPiP15HIP_vector_typeIfLj2EE
		.amdhsa_group_segment_fixed_size 126976
		.amdhsa_private_segment_fixed_size 0
		.amdhsa_kernarg_size 56
		.amdhsa_user_sgpr_count 2
		.amdhsa_user_sgpr_dispatch_ptr 0
		.amdhsa_user_sgpr_queue_ptr 0
		.amdhsa_user_sgpr_kernarg_segment_ptr 1
		.amdhsa_user_sgpr_dispatch_id 0
		.amdhsa_user_sgpr_kernarg_preload_length 0
		.amdhsa_user_sgpr_kernarg_preload_offset 0
		.amdhsa_user_sgpr_private_segment_size 0
		.amdhsa_uses_dynamic_stack 0
		.amdhsa_enable_private_segment 0
		.amdhsa_system_sgpr_workgroup_id_x 1
		.amdhsa_system_sgpr_workgroup_id_y 0
		.amdhsa_system_sgpr_workgroup_id_z 0
		.amdhsa_system_sgpr_workgroup_info 0
		.amdhsa_system_vgpr_workitem_id 0
		.amdhsa_next_free_vgpr 248
		.amdhsa_next_free_sgpr 96
		.amdhsa_accum_offset 248
		.amdhsa_reserve_vcc 1
		.amdhsa_float_round_mode_32 0
		.amdhsa_float_round_mode_16_64 0
		.amdhsa_float_denorm_mode_32 3
		.amdhsa_float_denorm_mode_16_64 3
		.amdhsa_dx10_clamp 1
		.amdhsa_ieee_mode 1
		.amdhsa_fp16_overflow 0
		.amdhsa_tg_split 0
		.amdhsa_exception_fp_ieee_invalid_op 0
		.amdhsa_exception_fp_denorm_src 0
		.amdhsa_exception_fp_ieee_div_zero 0
		.amdhsa_exception_fp_ieee_overflow 0
		.amdhsa_exception_fp_ieee_underflow 0
		.amdhsa_exception_fp_ieee_inexact 0
		.amdhsa_exception_int_div_zero 0
	.end_amdhsa_kernel

amdhsa.kernels:
  - .agpr_count:     0
    .args:
      - .actual_access:  read_only
        .address_space:  global
        .offset:         0
        .size:           8
        .value_kind:     global_buffer
      - .actual_access:  read_only
        .address_space:  global
        .offset:         8
        .size:           8
        .value_kind:     global_buffer
      - .actual_access:  read_only
        .address_space:  global
        .offset:         16
        .size:           8
        .value_kind:     global_buffer
      - .actual_access:  write_only
        .address_space:  global
        .offset:         24
        .size:           8
        .value_kind:     global_buffer
      - .actual_access:  write_only
        .address_space:  global
        .offset:         32
        .size:           8
        .value_kind:     global_buffer
      - .actual_access:  write_only
        .address_space:  global
        .offset:         40
        .size:           8
        .value_kind:     global_buffer
      - .actual_access:  write_only
        .address_space:  global
        .offset:         48
        .size:           8
        .value_kind:     global_buffer
      - .actual_access:  write_only
        .address_space:  global
        .offset:         56
        .size:           8
        .value_kind:     global_buffer
      - .actual_access:  write_only
        .address_space:  global
        .offset:         64
        .size:           8
        .value_kind:     global_buffer
      - .actual_access:  write_only
        .address_space:  global
        .offset:         72
        .size:           8
        .value_kind:     global_buffer
      - .actual_access:  write_only
        .address_space:  global
        .offset:         80
        .size:           8
        .value_kind:     global_buffer
    .group_segment_fixed_size: 49152
    .kernarg_segment_align: 8
    .kernarg_segment_size: 88
    .language:       OpenCL C
    .language_version:
      - 2
      - 0
    .max_flat_workgroup_size: 256
    .name:           _Z12quant_kernelPKfS0_PKiPhS3_PjS4_PfS5_S5_Pi
    .private_segment_fixed_size: 0
    .sgpr_count:     31
    .sgpr_spill_count: 0
    .symbol:         _Z12quant_kernelPKfS0_PKiPhS3_PjS4_PfS5_S5_Pi.kd
    .uniform_work_group_size: 1
    .uses_dynamic_stack: false
    .vgpr_count:     163
    .vgpr_spill_count: 0
    .wavefront_size: 64
  - .agpr_count:     0
    .args:
      - .actual_access:  read_only
        .address_space:  global
        .offset:         0
        .size:           8
        .value_kind:     global_buffer
      - .actual_access:  read_only
        .address_space:  global
        .offset:         8
        .size:           8
        .value_kind:     global_buffer
      - .address_space:  global
        .offset:         16
        .size:           8
        .value_kind:     global_buffer
      - .address_space:  global
        .offset:         24
        .size:           8
        .value_kind:     global_buffer
      - .address_space:  global
        .offset:         32
        .size:           8
        .value_kind:     global_buffer
      - .address_space:  global
        .offset:         40
        .size:           8
        .value_kind:     global_buffer
      - .actual_access:  write_only
        .address_space:  global
        .offset:         48
        .size:           8
        .value_kind:     global_buffer
    .group_segment_fixed_size: 126976
    .kernarg_segment_align: 8
    .kernarg_segment_size: 56
    .language:       OpenCL C
    .language_version:
      - 2
      - 0
    .max_flat_workgroup_size: 512
    .name:           _Z15gemm_lse_kernelPKhS0_PKjS2_PfPiP15HIP_vector_typeIfLj2EE
    .private_segment_fixed_size: 0
    .sgpr_count:     48
    .sgpr_spill_count: 0
    .symbol:         _Z15gemm_lse_kernelPKhS0_PKjS2_PfPiP15HIP_vector_typeIfLj2EE.kd
    .uniform_work_group_size: 1
    .uses_dynamic_stack: false
    .vgpr_count:     248
    .vgpr_spill_count: 0
    .wavefront_size: 64
  - .agpr_count:     0
    .args:
      - .actual_access:  read_only
        .address_space:  global
        .offset:         0
        .size:           8
        .value_kind:     global_buffer
      - .actual_access:  read_only
        .address_space:  global
        .offset:         8
        .size:           8
        .value_kind:     global_buffer
      - .actual_access:  read_only
        .address_space:  global
        .offset:         16
        .size:           8
        .value_kind:     global_buffer
      - .actual_access:  read_only
        .address_space:  global
        .offset:         24
        .size:           8
        .value_kind:     global_buffer
      - .actual_access:  read_only
        .address_space:  global
        .offset:         32
        .size:           8
        .value_kind:     global_buffer
      - .actual_access:  read_only
        .address_space:  global
        .offset:         40
        .size:           8
        .value_kind:     global_buffer
      - .address_space:  global
        .offset:         48
        .size:           8
        .value_kind:     global_buffer
    .group_segment_fixed_size: 16
    .kernarg_segment_align: 8
    .kernarg_segment_size: 56
    .language:       OpenCL C
    .language_version:
      - 2
      - 0
    .max_flat_workgroup_size: 256
    .name:           _Z15finalize_kernelPKfPKiPK15HIP_vector_typeIfLj2EES0_S2_S2_Pf
    .private_segment_fixed_size: 0
    .sgpr_count:     33
    .sgpr_spill_count: 0
    .symbol:         _Z15finalize_kernelPKfPKiPK15HIP_vector_typeIfLj2EES0_S2_S2_Pf.kd
    .uniform_work_group_size: 1
    .uses_dynamic_stack: false
    .vgpr_count:     19
    .vgpr_spill_count: 0
    .wavefront_size: 64
